# v27 + epilogue priority: leading half (waves 0-3) at prio 1 during GEMM epilogues, trailing half at prio 1 during the K-loops
# baseline (speedup 1.0000x reference)
.LBB0_390:
	s_andn2_b64 vcc, exec, s[48:49]
	s_cbranch_vccnz .Lprio_in
	s_setprio 1
	s_branch .Lpriod_in
.Lprio_in:
	s_setprio 0
.Lpriod_in:
	s_add_u32 s1, s42, 0x100
	v_lshl_add_u64 v[142:143], s[40:41], 0, v[130:131]
	s_addc_u32 s24, s43, 0
	s_mov_b32 s25, -2
	s_mov_b64 s[42:43], 0
	s_add_u32 s14, s40, s42
	s_addc_u32 s15, s41, s43
	s_add_u32 s34, s14, 0x100
	s_addc_u32 s35, s15, 0
	s_add_u32 s44, s1, s42
	s_addc_u32 s45, s24, s43
	s_cmpk_eq_i32 s42, 0x700
	s_cselect_b64 vcc, -1, 0
	s_and_b64 s[14:15], vcc, exec
	s_cselect_b32 s15, s55, s35
	s_cselect_b32 s14, s54, s34
	s_cselect_b32 s35, s69, s45
	s_cselect_b32 s34, s68, s44
	s_add_i32 s44, 0, 0x11000
	v_add_u32_e32 v145, s44, v1
	s_add_i32 s45, 0, 0x15000
	ds_read_b128 v[146:149], v145
	ds_read_b128 v[150:153], v145 offset:1024
	ds_read_b128 v[154:157], v145 offset:2048
	ds_read_b128 v[158:161], v145 offset:3072
	v_add_u32_e32 v145, s45, v1
	ds_read_b128 v[162:165], v145
	ds_read_b128 v[166:169], v145 offset:1024
	ds_read_b128 v[170:173], v145 offset:2048
	ds_read_b128 v[174:177], v145 offset:3072
	v_cndmask_b32_e32 v193, v131, v141, vcc
	v_cndmask_b32_e32 v192, v130, v140, vcc
	v_lshl_add_u64 v[220:221], v[142:143], 0, s[42:43]
	v_lshl_add_u64 v[222:223], v[220:221], 0, s[6:7]
	s_add_i32 m0, s28, 0xd000
	ds_read_b128 v[178:181], v144 offset:4096
	ds_read_b128 v[182:185], v144 offset:5120
	ds_read_b128 v[196:199], v144 offset:6144
	ds_read_b128 v[200:203], v144 offset:7168
	ds_read_b128 v[204:207], v144 offset:8192
	ds_read_b128 v[208:211], v144 offset:9216
	ds_read_b128 v[212:215], v144 offset:10240
	ds_read_b128 v[216:219], v144 offset:11264
	global_load_lds_dwordx4 v[222:223], off
	v_lshl_add_u64 v[220:221], v[220:221], 0, s[8:9]
	s_add_i32 m0, s28, 0xf000
	s_nop 0
	global_load_lds_dwordx4 v[220:221], off
	s_waitcnt vmcnt(8)
	s_waitcnt lgkmcnt(0)
	s_barrier
	s_waitcnt lgkmcnt(0)
	v_mfma_f32_16x16x32_bf16 v[126:129], v[146:149], v[178:181], 0
	v_mfma_f32_16x16x32_bf16 v[122:125], v[154:157], v[178:181], 0
	v_mfma_f32_16x16x32_bf16 v[110:113], v[146:149], v[196:199], 0
	v_mfma_f32_16x16x32_bf16 v[106:109], v[154:157], v[196:199], 0
	v_mfma_f32_16x16x32_bf16 v[94:97], v[146:149], v[204:207], 0
	v_mfma_f32_16x16x32_bf16 v[90:93], v[154:157], v[204:207], 0
	v_mfma_f32_16x16x32_bf16 v[78:81], v[146:149], v[212:215], 0
	v_mfma_f32_16x16x32_bf16 v[74:77], v[154:157], v[212:215], 0
	v_mfma_f32_16x16x32_bf16 v[126:129], v[150:153], v[182:185], v[126:129]
	v_mfma_f32_16x16x32_bf16 v[122:125], v[158:161], v[182:185], v[122:125]
	v_mfma_f32_16x16x32_bf16 v[110:113], v[150:153], v[200:203], v[110:113]
	v_mfma_f32_16x16x32_bf16 v[106:109], v[158:161], v[200:203], v[106:109]
	v_mfma_f32_16x16x32_bf16 v[94:97], v[150:153], v[208:211], v[94:97]
	v_mfma_f32_16x16x32_bf16 v[90:93], v[158:161], v[208:211], v[90:93]
	v_mfma_f32_16x16x32_bf16 v[78:81], v[150:153], v[216:219], v[78:81]
	v_mfma_f32_16x16x32_bf16 v[74:77], v[158:161], v[216:219], v[74:77]
	v_mfma_f32_16x16x32_bf16 v[118:121], v[162:165], v[178:181], 0
	v_mfma_f32_16x16x32_bf16 v[114:117], v[170:173], v[178:181], 0
	v_mfma_f32_16x16x32_bf16 v[102:105], v[162:165], v[196:199], 0
	v_mfma_f32_16x16x32_bf16 v[98:101], v[170:173], v[196:199], 0
	v_mfma_f32_16x16x32_bf16 v[86:89], v[162:165], v[204:207], 0
	v_mfma_f32_16x16x32_bf16 v[82:85], v[170:173], v[204:207], 0
	v_mfma_f32_16x16x32_bf16 v[70:73], v[162:165], v[212:215], 0
	v_mfma_f32_16x16x32_bf16 v[66:69], v[170:173], v[212:215], 0
	v_mfma_f32_16x16x32_bf16 v[118:121], v[166:169], v[182:185], v[118:121]
	v_mfma_f32_16x16x32_bf16 v[114:117], v[174:177], v[182:185], v[114:117]
	v_mfma_f32_16x16x32_bf16 v[102:105], v[166:169], v[200:203], v[102:105]
	v_mfma_f32_16x16x32_bf16 v[98:101], v[174:177], v[200:203], v[98:101]
	v_mfma_f32_16x16x32_bf16 v[86:89], v[166:169], v[208:211], v[86:89]
	v_mfma_f32_16x16x32_bf16 v[82:85], v[174:177], v[208:211], v[82:85]
	v_mfma_f32_16x16x32_bf16 v[70:73], v[166:169], v[216:219], v[70:73]
	v_mfma_f32_16x16x32_bf16 v[66:69], v[174:177], v[216:219], v[66:69]
	s_barrier
	s_add_i32 s44, s44, s12
	v_lshl_add_u64 v[220:221], s[34:35], 0, v[186:187]
	s_mov_b32 m0, s44
	ds_read_b128 v[178:181], v144 offset:20480
	ds_read_b128 v[182:185], v144 offset:21504
	ds_read_b128 v[196:199], v144 offset:22528
	ds_read_b128 v[200:203], v144 offset:23552
	ds_read_b128 v[204:207], v144 offset:24576
	ds_read_b128 v[208:211], v144 offset:25600
	ds_read_b128 v[212:215], v144 offset:26624
	ds_read_b128 v[216:219], v144 offset:27648
	global_load_lds_dwordx4 v186, s[34:35]
	v_lshl_add_u64 v[222:223], v[220:221], 0, s[82:83]
	s_add_i32 m0, s44, 0x2000
	s_add_i32 s34, s45, s12
	global_load_lds_dwordx4 v[222:223], off
	v_lshl_add_u64 v[222:223], v[220:221], 0, s[64:65]
	s_mov_b32 m0, s34
	v_lshl_add_u64 v[192:193], s[14:15], 0, v[192:193]
	global_load_lds_dwordx4 v[222:223], off
	v_lshl_add_u64 v[222:223], v[220:221], 0, s[86:87]
	s_add_i32 m0, s34, 0x2000
	s_nop 0
	global_load_lds_dwordx4 v[222:223], off
	s_mov_b32 m0, s29
	v_lshl_add_u64 v[222:223], v[192:193], 0, s[82:83]
	global_load_lds_dwordx4 v[192:193], off
	s_mov_b32 m0, s47
	s_nop 0
	global_load_lds_dwordx4 v[222:223], off
	s_waitcnt vmcnt(8)
	s_waitcnt lgkmcnt(0)
	s_barrier
	s_waitcnt lgkmcnt(0)
	v_mfma_f32_16x16x32_bf16 v[62:65], v[146:149], v[178:181], 0
	v_mfma_f32_16x16x32_bf16 v[58:61], v[154:157], v[178:181], 0
	v_mfma_f32_16x16x32_bf16 v[46:49], v[146:149], v[196:199], 0
	v_mfma_f32_16x16x32_bf16 v[42:45], v[154:157], v[196:199], 0
	v_mfma_f32_16x16x32_bf16 v[30:33], v[146:149], v[204:207], 0
	v_mfma_f32_16x16x32_bf16 v[26:29], v[154:157], v[204:207], 0
	v_mfma_f32_16x16x32_bf16 v[14:17], v[146:149], v[212:215], 0
	v_mfma_f32_16x16x32_bf16 v[10:13], v[154:157], v[212:215], 0
	v_mfma_f32_16x16x32_bf16 v[62:65], v[150:153], v[182:185], v[62:65]
	v_mfma_f32_16x16x32_bf16 v[58:61], v[158:161], v[182:185], v[58:61]
	v_mfma_f32_16x16x32_bf16 v[46:49], v[150:153], v[200:203], v[46:49]
	v_mfma_f32_16x16x32_bf16 v[42:45], v[158:161], v[200:203], v[42:45]
	v_mfma_f32_16x16x32_bf16 v[30:33], v[150:153], v[208:211], v[30:33]
	v_mfma_f32_16x16x32_bf16 v[26:29], v[158:161], v[208:211], v[26:29]
	v_mfma_f32_16x16x32_bf16 v[14:17], v[150:153], v[216:219], v[14:17]
	v_mfma_f32_16x16x32_bf16 v[10:13], v[158:161], v[216:219], v[10:13]
	v_mfma_f32_16x16x32_bf16 v[54:57], v[162:165], v[178:181], 0
	v_mfma_f32_16x16x32_bf16 v[50:53], v[170:173], v[178:181], 0
	v_mfma_f32_16x16x32_bf16 v[38:41], v[162:165], v[196:199], 0
	v_mfma_f32_16x16x32_bf16 v[34:37], v[170:173], v[196:199], 0
	v_mfma_f32_16x16x32_bf16 v[22:25], v[162:165], v[204:207], 0
	v_mfma_f32_16x16x32_bf16 v[18:21], v[170:173], v[204:207], 0
	v_mfma_f32_16x16x32_bf16 v[6:9], v[162:165], v[212:215], 0
	v_mfma_f32_16x16x32_bf16 v[2:5], v[170:173], v[212:215], 0
	v_mfma_f32_16x16x32_bf16 v[54:57], v[166:169], v[182:185], v[54:57]
	v_mfma_f32_16x16x32_bf16 v[50:53], v[174:177], v[182:185], v[50:53]
	v_mfma_f32_16x16x32_bf16 v[38:41], v[166:169], v[200:203], v[38:41]
	v_mfma_f32_16x16x32_bf16 v[34:37], v[174:177], v[200:203], v[34:37]
	v_mfma_f32_16x16x32_bf16 v[22:25], v[166:169], v[208:211], v[22:25]
	v_mfma_f32_16x16x32_bf16 v[18:21], v[174:177], v[208:211], v[18:21]
	v_mfma_f32_16x16x32_bf16 v[6:9], v[166:169], v[216:219], v[6:9]
	v_mfma_f32_16x16x32_bf16 v[2:5], v[174:177], v[216:219], v[2:5]
	s_barrier
	s_add_i32 s14, 0, 0x19000
	v_add_u32_e32 v145, s14, v1
	s_add_i32 s15, 0, 0x1d000
	ds_read_b128 v[146:149], v145
	ds_read_b128 v[150:153], v145 offset:1024
	ds_read_b128 v[154:157], v145 offset:2048
	ds_read_b128 v[158:161], v145 offset:3072
	v_add_u32_e32 v145, s15, v1
	ds_read_b128 v[162:165], v145
	ds_read_b128 v[166:169], v145 offset:1024
	ds_read_b128 v[170:173], v145 offset:2048
	ds_read_b128 v[174:177], v145 offset:3072
	s_mov_b32 m0, s60
	v_lshl_add_u64 v[222:223], v[192:193], 0, s[64:65]
	ds_read_b128 v[178:181], v144 offset:36864
	ds_read_b128 v[182:185], v144 offset:37888
	ds_read_b128 v[196:199], v144 offset:38912
	ds_read_b128 v[200:203], v144 offset:39936
	ds_read_b128 v[204:207], v144 offset:40960
	ds_read_b128 v[208:211], v144 offset:41984
	ds_read_b128 v[212:215], v144 offset:43008
	ds_read_b128 v[216:219], v144 offset:44032
	global_load_lds_dwordx4 v[222:223], off
	v_lshl_add_u64 v[222:223], v[192:193], 0, s[86:87]
	s_mov_b32 m0, s61
	s_nop 0
	global_load_lds_dwordx4 v[222:223], off
	s_waitcnt vmcnt(8)
	s_waitcnt lgkmcnt(0)
	s_barrier
	s_waitcnt lgkmcnt(0)
	v_mfma_f32_16x16x32_bf16 v[126:129], v[146:149], v[178:181], v[126:129]
	v_mfma_f32_16x16x32_bf16 v[122:125], v[154:157], v[178:181], v[122:125]
	v_mfma_f32_16x16x32_bf16 v[110:113], v[146:149], v[196:199], v[110:113]
	v_mfma_f32_16x16x32_bf16 v[106:109], v[154:157], v[196:199], v[106:109]
	v_mfma_f32_16x16x32_bf16 v[94:97], v[146:149], v[204:207], v[94:97]
	v_mfma_f32_16x16x32_bf16 v[90:93], v[154:157], v[204:207], v[90:93]
	v_mfma_f32_16x16x32_bf16 v[78:81], v[146:149], v[212:215], v[78:81]
	v_mfma_f32_16x16x32_bf16 v[74:77], v[154:157], v[212:215], v[74:77]
	v_mfma_f32_16x16x32_bf16 v[126:129], v[150:153], v[182:185], v[126:129]
	v_mfma_f32_16x16x32_bf16 v[122:125], v[158:161], v[182:185], v[122:125]
	v_mfma_f32_16x16x32_bf16 v[110:113], v[150:153], v[200:203], v[110:113]
	v_mfma_f32_16x16x32_bf16 v[106:109], v[158:161], v[200:203], v[106:109]
	v_mfma_f32_16x16x32_bf16 v[94:97], v[150:153], v[208:211], v[94:97]
	v_mfma_f32_16x16x32_bf16 v[90:93], v[158:161], v[208:211], v[90:93]
	v_mfma_f32_16x16x32_bf16 v[78:81], v[150:153], v[216:219], v[78:81]
	v_mfma_f32_16x16x32_bf16 v[74:77], v[158:161], v[216:219], v[74:77]
	v_mfma_f32_16x16x32_bf16 v[118:121], v[162:165], v[178:181], v[118:121]
	v_mfma_f32_16x16x32_bf16 v[114:117], v[170:173], v[178:181], v[114:117]
	v_mfma_f32_16x16x32_bf16 v[102:105], v[162:165], v[196:199], v[102:105]
	v_mfma_f32_16x16x32_bf16 v[98:101], v[170:173], v[196:199], v[98:101]
	v_mfma_f32_16x16x32_bf16 v[86:89], v[162:165], v[204:207], v[86:89]
	v_mfma_f32_16x16x32_bf16 v[82:85], v[170:173], v[204:207], v[82:85]
	v_mfma_f32_16x16x32_bf16 v[70:73], v[162:165], v[212:215], v[70:73]
	v_mfma_f32_16x16x32_bf16 v[66:69], v[170:173], v[212:215], v[66:69]
	v_mfma_f32_16x16x32_bf16 v[118:121], v[166:169], v[182:185], v[118:121]
	v_mfma_f32_16x16x32_bf16 v[114:117], v[174:177], v[182:185], v[114:117]
	v_mfma_f32_16x16x32_bf16 v[102:105], v[166:169], v[200:203], v[102:105]
	v_mfma_f32_16x16x32_bf16 v[98:101], v[174:177], v[200:203], v[98:101]
	v_mfma_f32_16x16x32_bf16 v[86:89], v[166:169], v[208:211], v[86:89]
	v_mfma_f32_16x16x32_bf16 v[82:85], v[174:177], v[208:211], v[82:85]
	v_mfma_f32_16x16x32_bf16 v[70:73], v[166:169], v[216:219], v[70:73]
	v_mfma_f32_16x16x32_bf16 v[66:69], v[174:177], v[216:219], v[66:69]
	s_barrier
	s_add_i32 s14, s14, s12
	v_lshl_add_u64 v[222:223], v[220:221], 0, s[92:93]
	s_mov_b32 m0, s14
	ds_read_b128 v[178:181], v144 offset:53248
	ds_read_b128 v[182:185], v144 offset:54272
	ds_read_b128 v[196:199], v144 offset:55296
	ds_read_b128 v[200:203], v144 offset:56320
	ds_read_b128 v[204:207], v144 offset:57344
	ds_read_b128 v[208:211], v144 offset:58368
	ds_read_b128 v[212:215], v144 offset:59392
	ds_read_b128 v[216:219], v144 offset:60416
	global_load_lds_dwordx4 v[222:223], off
	v_lshl_add_u64 v[222:223], v[220:221], 0, s[4:5]
	s_add_i32 m0, s14, 0x2000
	s_add_i32 s14, s15, s12
	global_load_lds_dwordx4 v[222:223], off
	v_lshl_add_u64 v[222:223], v[220:221], 0, s[6:7]
	s_mov_b32 m0, s14
	v_lshl_add_u64 v[220:221], v[220:221], 0, s[8:9]
	global_load_lds_dwordx4 v[222:223], off
	s_add_i32 m0, s14, 0x2000
	s_nop 0
	global_load_lds_dwordx4 v[220:221], off
	v_lshl_add_u64 v[220:221], v[192:193], 0, s[92:93]
	s_mov_b32 m0, s76
	v_lshl_add_u64 v[192:193], v[192:193], 0, s[4:5]
	global_load_lds_dwordx4 v[220:221], off
	s_mov_b32 m0, s77
	s_nop 0
	global_load_lds_dwordx4 v[192:193], off
	s_waitcnt vmcnt(8)
	s_waitcnt lgkmcnt(0)
	s_barrier
	s_waitcnt lgkmcnt(0)
	v_mfma_f32_16x16x32_bf16 v[62:65], v[146:149], v[178:181], v[62:65]
	v_mfma_f32_16x16x32_bf16 v[58:61], v[154:157], v[178:181], v[58:61]
	s_add_i32 s25, s25, 2
	v_mfma_f32_16x16x32_bf16 v[46:49], v[146:149], v[196:199], v[46:49]
	s_add_u32 s42, s42, 0x100
	v_mfma_f32_16x16x32_bf16 v[42:45], v[154:157], v[196:199], v[42:45]
	s_addc_u32 s43, s43, 0
	v_mfma_f32_16x16x32_bf16 v[30:33], v[146:149], v[204:207], v[30:33]
	s_add_u32 s14, s40, s42
	v_mfma_f32_16x16x32_bf16 v[26:29], v[154:157], v[204:207], v[26:29]
	s_addc_u32 s15, s41, s43
	v_mfma_f32_16x16x32_bf16 v[14:17], v[146:149], v[212:215], v[14:17]
	s_add_u32 s34, s14, 0x100
	v_mfma_f32_16x16x32_bf16 v[10:13], v[154:157], v[212:215], v[10:13]
	s_addc_u32 s35, s15, 0
	v_mfma_f32_16x16x32_bf16 v[62:65], v[150:153], v[182:185], v[62:65]
	s_add_u32 s44, s1, s42
	v_mfma_f32_16x16x32_bf16 v[58:61], v[158:161], v[182:185], v[58:61]
	s_addc_u32 s45, s24, s43
	v_mfma_f32_16x16x32_bf16 v[46:49], v[150:153], v[200:203], v[46:49]
	s_cmpk_eq_i32 s42, 0x700
	v_mfma_f32_16x16x32_bf16 v[42:45], v[158:161], v[200:203], v[42:45]
	s_cselect_b64 vcc, -1, 0
	v_mfma_f32_16x16x32_bf16 v[30:33], v[150:153], v[208:211], v[30:33]
	s_and_b64 s[14:15], vcc, exec
	v_mfma_f32_16x16x32_bf16 v[26:29], v[158:161], v[208:211], v[26:29]
	s_cselect_b32 s15, s55, s35
	v_mfma_f32_16x16x32_bf16 v[14:17], v[150:153], v[216:219], v[14:17]
	s_cselect_b32 s14, s54, s34
	v_mfma_f32_16x16x32_bf16 v[10:13], v[158:161], v[216:219], v[10:13]
	s_cselect_b32 s35, s69, s45
	v_mfma_f32_16x16x32_bf16 v[54:57], v[162:165], v[178:181], v[54:57]
	s_cselect_b32 s34, s68, s44
	v_mfma_f32_16x16x32_bf16 v[50:53], v[170:173], v[178:181], v[50:53]
	s_add_i32 s44, 0, 0x11000
	v_mfma_f32_16x16x32_bf16 v[38:41], v[162:165], v[196:199], v[38:41]
	s_add_i32 s45, 0, 0x15000
	v_mfma_f32_16x16x32_bf16 v[34:37], v[170:173], v[196:199], v[34:37]
	v_mfma_f32_16x16x32_bf16 v[22:25], v[162:165], v[204:207], v[22:25]
	v_mfma_f32_16x16x32_bf16 v[18:21], v[170:173], v[204:207], v[18:21]
	v_mfma_f32_16x16x32_bf16 v[6:9], v[162:165], v[212:215], v[6:9]
	v_mfma_f32_16x16x32_bf16 v[2:5], v[170:173], v[212:215], v[2:5]
	v_mfma_f32_16x16x32_bf16 v[54:57], v[166:169], v[182:185], v[54:57]
	v_mfma_f32_16x16x32_bf16 v[50:53], v[174:177], v[182:185], v[50:53]
	v_mfma_f32_16x16x32_bf16 v[38:41], v[166:169], v[200:203], v[38:41]
	v_mfma_f32_16x16x32_bf16 v[34:37], v[174:177], v[200:203], v[34:37]
	v_mfma_f32_16x16x32_bf16 v[22:25], v[166:169], v[208:211], v[22:25]
	v_mfma_f32_16x16x32_bf16 v[18:21], v[174:177], v[208:211], v[18:21]
	v_mfma_f32_16x16x32_bf16 v[6:9], v[166:169], v[216:219], v[6:9]
	v_mfma_f32_16x16x32_bf16 v[2:5], v[174:177], v[216:219], v[2:5]
	s_barrier
.LBB0_391:
	v_add_u32_e32 v145, s44, v1
	ds_read_b128 v[146:149], v145
	ds_read_b128 v[150:153], v145 offset:1024
	ds_read_b128 v[154:157], v145 offset:2048
	ds_read_b128 v[158:161], v145 offset:3072
	v_add_u32_e32 v145, s45, v1
	ds_read_b128 v[162:165], v145
	ds_read_b128 v[166:169], v145 offset:1024
	ds_read_b128 v[170:173], v145 offset:2048
	ds_read_b128 v[174:177], v145 offset:3072
	v_cndmask_b32_e32 v193, v131, v141, vcc
	v_cndmask_b32_e32 v192, v130, v140, vcc
	v_lshl_add_u64 v[220:221], v[142:143], 0, s[42:43]
	v_lshl_add_u64 v[222:223], v[220:221], 0, s[6:7]
	s_add_i32 m0, s28, 0xd000
	ds_read_b128 v[178:181], v144 offset:4096
	ds_read_b128 v[182:185], v144 offset:5120
	ds_read_b128 v[196:199], v144 offset:6144
	ds_read_b128 v[200:203], v144 offset:7168
	ds_read_b128 v[204:207], v144 offset:8192
	ds_read_b128 v[208:211], v144 offset:9216
	ds_read_b128 v[212:215], v144 offset:10240
	ds_read_b128 v[216:219], v144 offset:11264
	global_load_lds_dwordx4 v[222:223], off
	v_lshl_add_u64 v[220:221], v[220:221], 0, s[8:9]
	s_add_i32 m0, s28, 0xf000
	s_nop 0
	global_load_lds_dwordx4 v[220:221], off
	s_waitcnt vmcnt(8)
	s_waitcnt lgkmcnt(0)
	s_barrier
	s_waitcnt lgkmcnt(0)
	v_mfma_f32_16x16x32_bf16 v[126:129], v[146:149], v[178:181], v[126:129]
	v_mfma_f32_16x16x32_bf16 v[122:125], v[154:157], v[178:181], v[122:125]
	v_mfma_f32_16x16x32_bf16 v[110:113], v[146:149], v[196:199], v[110:113]
	v_mfma_f32_16x16x32_bf16 v[106:109], v[154:157], v[196:199], v[106:109]
	v_mfma_f32_16x16x32_bf16 v[94:97], v[146:149], v[204:207], v[94:97]
	v_mfma_f32_16x16x32_bf16 v[90:93], v[154:157], v[204:207], v[90:93]
	v_mfma_f32_16x16x32_bf16 v[78:81], v[146:149], v[212:215], v[78:81]
	v_mfma_f32_16x16x32_bf16 v[74:77], v[154:157], v[212:215], v[74:77]
	v_mfma_f32_16x16x32_bf16 v[126:129], v[150:153], v[182:185], v[126:129]
	v_mfma_f32_16x16x32_bf16 v[122:125], v[158:161], v[182:185], v[122:125]
	v_mfma_f32_16x16x32_bf16 v[110:113], v[150:153], v[200:203], v[110:113]
	v_mfma_f32_16x16x32_bf16 v[106:109], v[158:161], v[200:203], v[106:109]
	v_mfma_f32_16x16x32_bf16 v[94:97], v[150:153], v[208:211], v[94:97]
	v_mfma_f32_16x16x32_bf16 v[90:93], v[158:161], v[208:211], v[90:93]
	v_mfma_f32_16x16x32_bf16 v[78:81], v[150:153], v[216:219], v[78:81]
	v_mfma_f32_16x16x32_bf16 v[74:77], v[158:161], v[216:219], v[74:77]
	v_mfma_f32_16x16x32_bf16 v[118:121], v[162:165], v[178:181], v[118:121]
	v_mfma_f32_16x16x32_bf16 v[114:117], v[170:173], v[178:181], v[114:117]
	v_mfma_f32_16x16x32_bf16 v[102:105], v[162:165], v[196:199], v[102:105]
	v_mfma_f32_16x16x32_bf16 v[98:101], v[170:173], v[196:199], v[98:101]
	v_mfma_f32_16x16x32_bf16 v[86:89], v[162:165], v[204:207], v[86:89]
	v_mfma_f32_16x16x32_bf16 v[82:85], v[170:173], v[204:207], v[82:85]
	v_mfma_f32_16x16x32_bf16 v[70:73], v[162:165], v[212:215], v[70:73]
	v_mfma_f32_16x16x32_bf16 v[66:69], v[170:173], v[212:215], v[66:69]
	v_mfma_f32_16x16x32_bf16 v[118:121], v[166:169], v[182:185], v[118:121]
	v_mfma_f32_16x16x32_bf16 v[114:117], v[174:177], v[182:185], v[114:117]
	v_mfma_f32_16x16x32_bf16 v[102:105], v[166:169], v[200:203], v[102:105]
	v_mfma_f32_16x16x32_bf16 v[98:101], v[174:177], v[200:203], v[98:101]
	v_mfma_f32_16x16x32_bf16 v[86:89], v[166:169], v[208:211], v[86:89]
	v_mfma_f32_16x16x32_bf16 v[82:85], v[174:177], v[208:211], v[82:85]
	v_mfma_f32_16x16x32_bf16 v[70:73], v[166:169], v[216:219], v[70:73]
	v_mfma_f32_16x16x32_bf16 v[66:69], v[174:177], v[216:219], v[66:69]
	s_barrier
	s_add_i32 s44, s44, s12
	v_lshl_add_u64 v[220:221], s[34:35], 0, v[186:187]
	s_mov_b32 m0, s44
	ds_read_b128 v[178:181], v144 offset:20480
	ds_read_b128 v[182:185], v144 offset:21504
	ds_read_b128 v[196:199], v144 offset:22528
	ds_read_b128 v[200:203], v144 offset:23552
	ds_read_b128 v[204:207], v144 offset:24576
	ds_read_b128 v[208:211], v144 offset:25600
	ds_read_b128 v[212:215], v144 offset:26624
	ds_read_b128 v[216:219], v144 offset:27648
	global_load_lds_dwordx4 v186, s[34:35]
	v_lshl_add_u64 v[222:223], v[220:221], 0, s[82:83]
	s_add_i32 m0, s44, 0x2000
	s_add_i32 s34, s45, s12
	global_load_lds_dwordx4 v[222:223], off
	v_lshl_add_u64 v[222:223], v[220:221], 0, s[64:65]
	s_mov_b32 m0, s34
	v_lshl_add_u64 v[192:193], s[14:15], 0, v[192:193]
	global_load_lds_dwordx4 v[222:223], off
	v_lshl_add_u64 v[222:223], v[220:221], 0, s[86:87]
	s_add_i32 m0, s34, 0x2000
	s_nop 0
	global_load_lds_dwordx4 v[222:223], off
	s_mov_b32 m0, s29
	v_lshl_add_u64 v[222:223], v[192:193], 0, s[82:83]
	global_load_lds_dwordx4 v[192:193], off
	s_mov_b32 m0, s47
	s_nop 0
	global_load_lds_dwordx4 v[222:223], off
	s_waitcnt vmcnt(8)
	s_waitcnt lgkmcnt(0)
	s_barrier
	s_waitcnt lgkmcnt(0)
	v_mfma_f32_16x16x32_bf16 v[62:65], v[146:149], v[178:181], v[62:65]
	v_mfma_f32_16x16x32_bf16 v[58:61], v[154:157], v[178:181], v[58:61]
	v_mfma_f32_16x16x32_bf16 v[46:49], v[146:149], v[196:199], v[46:49]
	v_mfma_f32_16x16x32_bf16 v[42:45], v[154:157], v[196:199], v[42:45]
	v_mfma_f32_16x16x32_bf16 v[30:33], v[146:149], v[204:207], v[30:33]
	v_mfma_f32_16x16x32_bf16 v[26:29], v[154:157], v[204:207], v[26:29]
	v_mfma_f32_16x16x32_bf16 v[14:17], v[146:149], v[212:215], v[14:17]
	v_mfma_f32_16x16x32_bf16 v[10:13], v[154:157], v[212:215], v[10:13]
	v_mfma_f32_16x16x32_bf16 v[62:65], v[150:153], v[182:185], v[62:65]
	v_mfma_f32_16x16x32_bf16 v[58:61], v[158:161], v[182:185], v[58:61]
	v_mfma_f32_16x16x32_bf16 v[46:49], v[150:153], v[200:203], v[46:49]
	v_mfma_f32_16x16x32_bf16 v[42:45], v[158:161], v[200:203], v[42:45]
	v_mfma_f32_16x16x32_bf16 v[30:33], v[150:153], v[208:211], v[30:33]
	v_mfma_f32_16x16x32_bf16 v[26:29], v[158:161], v[208:211], v[26:29]
	v_mfma_f32_16x16x32_bf16 v[14:17], v[150:153], v[216:219], v[14:17]
	v_mfma_f32_16x16x32_bf16 v[10:13], v[158:161], v[216:219], v[10:13]
	v_mfma_f32_16x16x32_bf16 v[54:57], v[162:165], v[178:181], v[54:57]
	v_mfma_f32_16x16x32_bf16 v[50:53], v[170:173], v[178:181], v[50:53]
	v_mfma_f32_16x16x32_bf16 v[38:41], v[162:165], v[196:199], v[38:41]
	v_mfma_f32_16x16x32_bf16 v[34:37], v[170:173], v[196:199], v[34:37]
	v_mfma_f32_16x16x32_bf16 v[22:25], v[162:165], v[204:207], v[22:25]
	v_mfma_f32_16x16x32_bf16 v[18:21], v[170:173], v[204:207], v[18:21]
	v_mfma_f32_16x16x32_bf16 v[6:9], v[162:165], v[212:215], v[6:9]
	v_mfma_f32_16x16x32_bf16 v[2:5], v[170:173], v[212:215], v[2:5]
	v_mfma_f32_16x16x32_bf16 v[54:57], v[166:169], v[182:185], v[54:57]
	v_mfma_f32_16x16x32_bf16 v[50:53], v[174:177], v[182:185], v[50:53]
	v_mfma_f32_16x16x32_bf16 v[38:41], v[166:169], v[200:203], v[38:41]
	v_mfma_f32_16x16x32_bf16 v[34:37], v[174:177], v[200:203], v[34:37]
	v_mfma_f32_16x16x32_bf16 v[22:25], v[166:169], v[208:211], v[22:25]
	v_mfma_f32_16x16x32_bf16 v[18:21], v[174:177], v[208:211], v[18:21]
	v_mfma_f32_16x16x32_bf16 v[6:9], v[166:169], v[216:219], v[6:9]
	v_mfma_f32_16x16x32_bf16 v[2:5], v[174:177], v[216:219], v[2:5]
	s_barrier
	s_add_i32 s14, 0, 0x19000
	v_add_u32_e32 v145, s14, v1
	s_add_i32 s15, 0, 0x1d000
	ds_read_b128 v[146:149], v145
	ds_read_b128 v[150:153], v145 offset:1024
	ds_read_b128 v[154:157], v145 offset:2048
	ds_read_b128 v[158:161], v145 offset:3072
	v_add_u32_e32 v145, s15, v1
	ds_read_b128 v[162:165], v145
	ds_read_b128 v[166:169], v145 offset:1024
	ds_read_b128 v[170:173], v145 offset:2048
	ds_read_b128 v[174:177], v145 offset:3072
	s_mov_b32 m0, s60
	v_lshl_add_u64 v[222:223], v[192:193], 0, s[64:65]
	ds_read_b128 v[178:181], v144 offset:36864
	ds_read_b128 v[182:185], v144 offset:37888
	ds_read_b128 v[196:199], v144 offset:38912
	ds_read_b128 v[200:203], v144 offset:39936
	ds_read_b128 v[204:207], v144 offset:40960
	ds_read_b128 v[208:211], v144 offset:41984
	ds_read_b128 v[212:215], v144 offset:43008
	ds_read_b128 v[216:219], v144 offset:44032
	global_load_lds_dwordx4 v[222:223], off
	v_lshl_add_u64 v[222:223], v[192:193], 0, s[86:87]
	s_mov_b32 m0, s61
	s_nop 0
	global_load_lds_dwordx4 v[222:223], off
	s_waitcnt vmcnt(8)
	s_waitcnt lgkmcnt(0)
	s_barrier
	s_waitcnt lgkmcnt(0)
	v_mfma_f32_16x16x32_bf16 v[126:129], v[146:149], v[178:181], v[126:129]
	v_mfma_f32_16x16x32_bf16 v[122:125], v[154:157], v[178:181], v[122:125]
	v_mfma_f32_16x16x32_bf16 v[110:113], v[146:149], v[196:199], v[110:113]
	v_mfma_f32_16x16x32_bf16 v[106:109], v[154:157], v[196:199], v[106:109]
	v_mfma_f32_16x16x32_bf16 v[94:97], v[146:149], v[204:207], v[94:97]
	v_mfma_f32_16x16x32_bf16 v[90:93], v[154:157], v[204:207], v[90:93]
	v_mfma_f32_16x16x32_bf16 v[78:81], v[146:149], v[212:215], v[78:81]
	v_mfma_f32_16x16x32_bf16 v[74:77], v[154:157], v[212:215], v[74:77]
	v_mfma_f32_16x16x32_bf16 v[126:129], v[150:153], v[182:185], v[126:129]
	v_mfma_f32_16x16x32_bf16 v[122:125], v[158:161], v[182:185], v[122:125]
	v_mfma_f32_16x16x32_bf16 v[110:113], v[150:153], v[200:203], v[110:113]
	v_mfma_f32_16x16x32_bf16 v[106:109], v[158:161], v[200:203], v[106:109]
	v_mfma_f32_16x16x32_bf16 v[94:97], v[150:153], v[208:211], v[94:97]
	v_mfma_f32_16x16x32_bf16 v[90:93], v[158:161], v[208:211], v[90:93]
	v_mfma_f32_16x16x32_bf16 v[78:81], v[150:153], v[216:219], v[78:81]
	v_mfma_f32_16x16x32_bf16 v[74:77], v[158:161], v[216:219], v[74:77]
	v_mfma_f32_16x16x32_bf16 v[118:121], v[162:165], v[178:181], v[118:121]
	v_mfma_f32_16x16x32_bf16 v[114:117], v[170:173], v[178:181], v[114:117]
	v_mfma_f32_16x16x32_bf16 v[102:105], v[162:165], v[196:199], v[102:105]
	v_mfma_f32_16x16x32_bf16 v[98:101], v[170:173], v[196:199], v[98:101]
	v_mfma_f32_16x16x32_bf16 v[86:89], v[162:165], v[204:207], v[86:89]
	v_mfma_f32_16x16x32_bf16 v[82:85], v[170:173], v[204:207], v[82:85]
	v_mfma_f32_16x16x32_bf16 v[70:73], v[162:165], v[212:215], v[70:73]
	v_mfma_f32_16x16x32_bf16 v[66:69], v[170:173], v[212:215], v[66:69]
	v_mfma_f32_16x16x32_bf16 v[118:121], v[166:169], v[182:185], v[118:121]
	v_mfma_f32_16x16x32_bf16 v[114:117], v[174:177], v[182:185], v[114:117]
	v_mfma_f32_16x16x32_bf16 v[102:105], v[166:169], v[200:203], v[102:105]
	v_mfma_f32_16x16x32_bf16 v[98:101], v[174:177], v[200:203], v[98:101]
	v_mfma_f32_16x16x32_bf16 v[86:89], v[166:169], v[208:211], v[86:89]
	v_mfma_f32_16x16x32_bf16 v[82:85], v[174:177], v[208:211], v[82:85]
	v_mfma_f32_16x16x32_bf16 v[70:73], v[166:169], v[216:219], v[70:73]
	v_mfma_f32_16x16x32_bf16 v[66:69], v[174:177], v[216:219], v[66:69]
	s_barrier
	s_add_i32 s14, s14, s12
	v_lshl_add_u64 v[222:223], v[220:221], 0, s[92:93]
	s_mov_b32 m0, s14
	ds_read_b128 v[178:181], v144 offset:53248
	ds_read_b128 v[182:185], v144 offset:54272
	ds_read_b128 v[196:199], v144 offset:55296
	ds_read_b128 v[200:203], v144 offset:56320
	ds_read_b128 v[204:207], v144 offset:57344
	ds_read_b128 v[208:211], v144 offset:58368
	ds_read_b128 v[212:215], v144 offset:59392
	ds_read_b128 v[216:219], v144 offset:60416
	global_load_lds_dwordx4 v[222:223], off
	v_lshl_add_u64 v[222:223], v[220:221], 0, s[4:5]
	s_add_i32 m0, s14, 0x2000
	s_add_i32 s14, s15, s12
	global_load_lds_dwordx4 v[222:223], off
	v_lshl_add_u64 v[222:223], v[220:221], 0, s[6:7]
	s_mov_b32 m0, s14
	v_lshl_add_u64 v[220:221], v[220:221], 0, s[8:9]
	global_load_lds_dwordx4 v[222:223], off
	s_add_i32 m0, s14, 0x2000
	s_nop 0
	global_load_lds_dwordx4 v[220:221], off
	v_lshl_add_u64 v[220:221], v[192:193], 0, s[92:93]
	s_mov_b32 m0, s76
	v_lshl_add_u64 v[192:193], v[192:193], 0, s[4:5]
	global_load_lds_dwordx4 v[220:221], off
	s_mov_b32 m0, s77
	s_nop 0
	global_load_lds_dwordx4 v[192:193], off
	s_waitcnt vmcnt(8)
	s_waitcnt lgkmcnt(0)
	s_barrier
	s_waitcnt lgkmcnt(0)
	v_mfma_f32_16x16x32_bf16 v[62:65], v[146:149], v[178:181], v[62:65]
	v_mfma_f32_16x16x32_bf16 v[58:61], v[154:157], v[178:181], v[58:61]
	s_add_i32 s25, s25, 2
	v_mfma_f32_16x16x32_bf16 v[46:49], v[146:149], v[196:199], v[46:49]
	s_add_u32 s42, s42, 0x100
	v_mfma_f32_16x16x32_bf16 v[42:45], v[154:157], v[196:199], v[42:45]
	s_addc_u32 s43, s43, 0
	v_mfma_f32_16x16x32_bf16 v[30:33], v[146:149], v[204:207], v[30:33]
	s_add_u32 s14, s40, s42
	v_mfma_f32_16x16x32_bf16 v[26:29], v[154:157], v[204:207], v[26:29]
	s_addc_u32 s15, s41, s43
	v_mfma_f32_16x16x32_bf16 v[14:17], v[146:149], v[212:215], v[14:17]
	s_add_u32 s34, s14, 0x100
	v_mfma_f32_16x16x32_bf16 v[10:13], v[154:157], v[212:215], v[10:13]
	s_addc_u32 s35, s15, 0
	v_mfma_f32_16x16x32_bf16 v[62:65], v[150:153], v[182:185], v[62:65]
	s_add_u32 s44, s1, s42
	v_mfma_f32_16x16x32_bf16 v[58:61], v[158:161], v[182:185], v[58:61]
	s_addc_u32 s45, s24, s43
	v_mfma_f32_16x16x32_bf16 v[46:49], v[150:153], v[200:203], v[46:49]
	s_cmpk_eq_i32 s42, 0x700
	v_mfma_f32_16x16x32_bf16 v[42:45], v[158:161], v[200:203], v[42:45]
	s_cselect_b64 vcc, -1, 0
	v_mfma_f32_16x16x32_bf16 v[30:33], v[150:153], v[208:211], v[30:33]
	s_and_b64 s[14:15], vcc, exec
	v_mfma_f32_16x16x32_bf16 v[26:29], v[158:161], v[208:211], v[26:29]
	s_cselect_b32 s15, s55, s35
	v_mfma_f32_16x16x32_bf16 v[14:17], v[150:153], v[216:219], v[14:17]
	s_cselect_b32 s14, s54, s34
	v_mfma_f32_16x16x32_bf16 v[10:13], v[158:161], v[216:219], v[10:13]
	s_cselect_b32 s35, s69, s45
	v_mfma_f32_16x16x32_bf16 v[54:57], v[162:165], v[178:181], v[54:57]
	s_cselect_b32 s34, s68, s44
	v_mfma_f32_16x16x32_bf16 v[50:53], v[170:173], v[178:181], v[50:53]
	s_add_i32 s44, 0, 0x11000
	v_mfma_f32_16x16x32_bf16 v[38:41], v[162:165], v[196:199], v[38:41]
	s_add_i32 s45, 0, 0x15000
	v_mfma_f32_16x16x32_bf16 v[34:37], v[170:173], v[196:199], v[34:37]
	v_mfma_f32_16x16x32_bf16 v[22:25], v[162:165], v[204:207], v[22:25]
	v_mfma_f32_16x16x32_bf16 v[18:21], v[170:173], v[204:207], v[18:21]
	v_mfma_f32_16x16x32_bf16 v[6:9], v[162:165], v[212:215], v[6:9]
	v_mfma_f32_16x16x32_bf16 v[2:5], v[170:173], v[212:215], v[2:5]
	v_mfma_f32_16x16x32_bf16 v[54:57], v[166:169], v[182:185], v[54:57]
	v_mfma_f32_16x16x32_bf16 v[50:53], v[174:177], v[182:185], v[50:53]
	v_mfma_f32_16x16x32_bf16 v[38:41], v[166:169], v[200:203], v[38:41]
	v_mfma_f32_16x16x32_bf16 v[34:37], v[174:177], v[200:203], v[34:37]
	v_mfma_f32_16x16x32_bf16 v[22:25], v[166:169], v[208:211], v[22:25]
	v_mfma_f32_16x16x32_bf16 v[18:21], v[174:177], v[208:211], v[18:21]
	v_mfma_f32_16x16x32_bf16 v[6:9], v[166:169], v[216:219], v[6:9]
	v_mfma_f32_16x16x32_bf16 v[2:5], v[174:177], v[216:219], v[2:5]
	s_barrier
	s_cmp_gt_u32 s25, 13
	s_cbranch_scc0 .LBB0_391
	s_and_b64 vcc, exec, s[48:49]
	s_cbranch_vccnz .Lepi1_in
	s_setprio 1
	s_branch .Lepid_in

.Lepid_in:
	s_and_b64 vcc, exec, s[50:51]
	s_cbranch_vccz .LBB0_394
	s_barrier

.LBB0_1110:
	s_andn2_b64 vcc, exec, s[0:1]
	s_cbranch_vccnz .Lprio_out
	s_setprio 1
	s_branch .Lpriod_out
.Lprio_out:
	s_setprio 0
.Lpriod_out:
	s_add_u32 s24, s54, 0x100
	v_lshl_add_u64 v[140:141], s[52:53], 0, v[138:139]
	s_addc_u32 s25, s55, 0
	s_mov_b32 s43, -2
	s_mov_b64 s[54:55], 0
	s_add_u32 s14, s52, s54
	s_addc_u32 s15, s53, s55
	s_add_u32 s45, s14, 0x100
	s_addc_u32 s73, s15, 0
	s_add_u32 s74, s24, s54
	s_addc_u32 s75, s25, s55
	s_cmpk_eq_i32 s54, 0x700
	s_cselect_b64 vcc, -1, 0
	s_and_b64 s[14:15], vcc, exec
	s_cselect_b32 s15, s47, s73
	s_cselect_b32 s14, s46, s45
	s_cselect_b32 s75, s49, s75
	s_cselect_b32 s74, s48, s74
	s_add_i32 s45, 0, 0x11000
	v_add_u32_e32 v131, s45, v1
	s_add_i32 s73, 0, 0x15000
	ds_read_b128 v[144:147], v131
	ds_read_b128 v[148:151], v131 offset:1024
	ds_read_b128 v[152:155], v131 offset:2048
	ds_read_b128 v[156:159], v131 offset:3072
	v_add_u32_e32 v131, s73, v1
	ds_read_b128 v[160:163], v131
	ds_read_b128 v[164:167], v131 offset:1024
	ds_read_b128 v[168:171], v131 offset:2048
	ds_read_b128 v[172:175], v131 offset:3072
	v_cndmask_b32_e32 v185, v139, v137, vcc
	v_cndmask_b32_e32 v184, v138, v136, vcc
	v_lshl_add_u64 v[192:193], v[140:141], 0, s[54:55]
	v_lshl_add_u64 v[220:221], v[192:193], 0, s[6:7]
	s_add_i32 m0, s29, 0xd000
	ds_read_b128 v[176:179], v142 offset:4096
	ds_read_b128 v[180:183], v142 offset:5120
	ds_read_b128 v[196:199], v142 offset:6144
	ds_read_b128 v[200:203], v142 offset:7168
	ds_read_b128 v[204:207], v142 offset:8192
	ds_read_b128 v[208:211], v142 offset:9216
	ds_read_b128 v[212:215], v142 offset:10240
	ds_read_b128 v[216:219], v142 offset:11264
	global_load_lds_dwordx4 v[220:221], off
	v_lshl_add_u64 v[192:193], v[192:193], 0, s[8:9]
	s_add_i32 m0, s29, 0xf000
	s_nop 0
	global_load_lds_dwordx4 v[192:193], off
	s_waitcnt vmcnt(8)
	s_waitcnt lgkmcnt(0)
	s_barrier
	s_waitcnt lgkmcnt(0)
	v_mfma_f32_16x16x32_bf16 v[126:129], v[144:147], v[176:179], 0
	v_mfma_f32_16x16x32_bf16 v[122:125], v[152:155], v[176:179], 0
	v_mfma_f32_16x16x32_bf16 v[110:113], v[144:147], v[196:199], 0
	v_mfma_f32_16x16x32_bf16 v[106:109], v[152:155], v[196:199], 0
	v_mfma_f32_16x16x32_bf16 v[94:97], v[144:147], v[204:207], 0
	v_mfma_f32_16x16x32_bf16 v[90:93], v[152:155], v[204:207], 0
	v_mfma_f32_16x16x32_bf16 v[78:81], v[144:147], v[212:215], 0
	v_mfma_f32_16x16x32_bf16 v[74:77], v[152:155], v[212:215], 0
	v_mfma_f32_16x16x32_bf16 v[126:129], v[148:151], v[180:183], v[126:129]
	v_mfma_f32_16x16x32_bf16 v[122:125], v[156:159], v[180:183], v[122:125]
	v_mfma_f32_16x16x32_bf16 v[110:113], v[148:151], v[200:203], v[110:113]
	v_mfma_f32_16x16x32_bf16 v[106:109], v[156:159], v[200:203], v[106:109]
	v_mfma_f32_16x16x32_bf16 v[94:97], v[148:151], v[208:211], v[94:97]
	v_mfma_f32_16x16x32_bf16 v[90:93], v[156:159], v[208:211], v[90:93]
	v_mfma_f32_16x16x32_bf16 v[78:81], v[148:151], v[216:219], v[78:81]
	v_mfma_f32_16x16x32_bf16 v[74:77], v[156:159], v[216:219], v[74:77]
	v_mfma_f32_16x16x32_bf16 v[118:121], v[160:163], v[176:179], 0
	v_mfma_f32_16x16x32_bf16 v[114:117], v[168:171], v[176:179], 0
	v_mfma_f32_16x16x32_bf16 v[102:105], v[160:163], v[196:199], 0
	v_mfma_f32_16x16x32_bf16 v[98:101], v[168:171], v[196:199], 0
	v_mfma_f32_16x16x32_bf16 v[86:89], v[160:163], v[204:207], 0
	v_mfma_f32_16x16x32_bf16 v[82:85], v[168:171], v[204:207], 0
	v_mfma_f32_16x16x32_bf16 v[70:73], v[160:163], v[212:215], 0
	v_mfma_f32_16x16x32_bf16 v[66:69], v[168:171], v[212:215], 0
	v_mfma_f32_16x16x32_bf16 v[118:121], v[164:167], v[180:183], v[118:121]
	v_mfma_f32_16x16x32_bf16 v[114:117], v[172:175], v[180:183], v[114:117]
	v_mfma_f32_16x16x32_bf16 v[102:105], v[164:167], v[200:203], v[102:105]
	v_mfma_f32_16x16x32_bf16 v[98:101], v[172:175], v[200:203], v[98:101]
	v_mfma_f32_16x16x32_bf16 v[86:89], v[164:167], v[208:211], v[86:89]
	v_mfma_f32_16x16x32_bf16 v[82:85], v[172:175], v[208:211], v[82:85]
	v_mfma_f32_16x16x32_bf16 v[70:73], v[164:167], v[216:219], v[70:73]
	v_mfma_f32_16x16x32_bf16 v[66:69], v[172:175], v[216:219], v[66:69]
	s_barrier
	s_add_i32 s45, s45, s2
	v_lshl_add_u64 v[192:193], s[74:75], 0, v[186:187]
	s_mov_b32 m0, s45
	ds_read_b128 v[176:179], v142 offset:20480
	ds_read_b128 v[180:183], v142 offset:21504
	ds_read_b128 v[196:199], v142 offset:22528
	ds_read_b128 v[200:203], v142 offset:23552
	ds_read_b128 v[204:207], v142 offset:24576
	ds_read_b128 v[208:211], v142 offset:25600
	ds_read_b128 v[212:215], v142 offset:26624
	ds_read_b128 v[216:219], v142 offset:27648
	global_load_lds_dwordx4 v186, s[74:75]
	v_lshl_add_u64 v[220:221], v[192:193], 0, s[82:83]
	s_add_i32 m0, s45, 0x2000
	s_add_i32 s45, s73, s2
	global_load_lds_dwordx4 v[220:221], off
	v_lshl_add_u64 v[220:221], v[192:193], 0, s[64:65]
	s_mov_b32 m0, s45
	v_lshl_add_u64 v[184:185], s[14:15], 0, v[184:185]
	global_load_lds_dwordx4 v[220:221], off
	v_lshl_add_u64 v[220:221], v[192:193], 0, s[86:87]
	s_add_i32 m0, s45, 0x2000
	s_nop 0
	global_load_lds_dwordx4 v[220:221], off
	s_mov_b32 m0, s33
	v_lshl_add_u64 v[220:221], v[184:185], 0, s[82:83]
	global_load_lds_dwordx4 v[184:185], off
	s_mov_b32 m0, s34
	s_nop 0
	global_load_lds_dwordx4 v[220:221], off
	s_waitcnt vmcnt(8)
	s_waitcnt lgkmcnt(0)
	s_barrier
	s_waitcnt lgkmcnt(0)
	v_mfma_f32_16x16x32_bf16 v[62:65], v[144:147], v[176:179], 0
	v_mfma_f32_16x16x32_bf16 v[58:61], v[152:155], v[176:179], 0
	v_mfma_f32_16x16x32_bf16 v[46:49], v[144:147], v[196:199], 0
	v_mfma_f32_16x16x32_bf16 v[42:45], v[152:155], v[196:199], 0
	v_mfma_f32_16x16x32_bf16 v[30:33], v[144:147], v[204:207], 0
	v_mfma_f32_16x16x32_bf16 v[26:29], v[152:155], v[204:207], 0
	v_mfma_f32_16x16x32_bf16 v[14:17], v[144:147], v[212:215], 0
	v_mfma_f32_16x16x32_bf16 v[10:13], v[152:155], v[212:215], 0
	v_mfma_f32_16x16x32_bf16 v[62:65], v[148:151], v[180:183], v[62:65]
	v_mfma_f32_16x16x32_bf16 v[58:61], v[156:159], v[180:183], v[58:61]
	v_mfma_f32_16x16x32_bf16 v[46:49], v[148:151], v[200:203], v[46:49]
	v_mfma_f32_16x16x32_bf16 v[42:45], v[156:159], v[200:203], v[42:45]
	v_mfma_f32_16x16x32_bf16 v[30:33], v[148:151], v[208:211], v[30:33]
	v_mfma_f32_16x16x32_bf16 v[26:29], v[156:159], v[208:211], v[26:29]
	v_mfma_f32_16x16x32_bf16 v[14:17], v[148:151], v[216:219], v[14:17]
	v_mfma_f32_16x16x32_bf16 v[10:13], v[156:159], v[216:219], v[10:13]
	v_mfma_f32_16x16x32_bf16 v[54:57], v[160:163], v[176:179], 0
	v_mfma_f32_16x16x32_bf16 v[50:53], v[168:171], v[176:179], 0
	v_mfma_f32_16x16x32_bf16 v[38:41], v[160:163], v[196:199], 0
	v_mfma_f32_16x16x32_bf16 v[34:37], v[168:171], v[196:199], 0
	v_mfma_f32_16x16x32_bf16 v[22:25], v[160:163], v[204:207], 0
	v_mfma_f32_16x16x32_bf16 v[18:21], v[168:171], v[204:207], 0
	v_mfma_f32_16x16x32_bf16 v[6:9], v[160:163], v[212:215], 0
	v_mfma_f32_16x16x32_bf16 v[2:5], v[168:171], v[212:215], 0
	v_mfma_f32_16x16x32_bf16 v[54:57], v[164:167], v[180:183], v[54:57]
	v_mfma_f32_16x16x32_bf16 v[50:53], v[172:175], v[180:183], v[50:53]
	v_mfma_f32_16x16x32_bf16 v[38:41], v[164:167], v[200:203], v[38:41]
	v_mfma_f32_16x16x32_bf16 v[34:37], v[172:175], v[200:203], v[34:37]
	v_mfma_f32_16x16x32_bf16 v[22:25], v[164:167], v[208:211], v[22:25]
	v_mfma_f32_16x16x32_bf16 v[18:21], v[172:175], v[208:211], v[18:21]
	v_mfma_f32_16x16x32_bf16 v[6:9], v[164:167], v[216:219], v[6:9]
	v_mfma_f32_16x16x32_bf16 v[2:5], v[172:175], v[216:219], v[2:5]
	s_barrier
	s_add_i32 s14, 0, 0x19000
	v_add_u32_e32 v131, s14, v1
	s_add_i32 s15, 0, 0x1d000
	ds_read_b128 v[144:147], v131
	ds_read_b128 v[148:151], v131 offset:1024
	ds_read_b128 v[152:155], v131 offset:2048
	ds_read_b128 v[156:159], v131 offset:3072
	v_add_u32_e32 v131, s15, v1
	ds_read_b128 v[160:163], v131
	ds_read_b128 v[164:167], v131 offset:1024
	ds_read_b128 v[168:171], v131 offset:2048
	ds_read_b128 v[172:175], v131 offset:3072
	s_mov_b32 m0, s35
	v_lshl_add_u64 v[220:221], v[184:185], 0, s[64:65]
	ds_read_b128 v[176:179], v142 offset:36864
	ds_read_b128 v[180:183], v142 offset:37888
	ds_read_b128 v[196:199], v142 offset:38912
	ds_read_b128 v[200:203], v142 offset:39936
	ds_read_b128 v[204:207], v142 offset:40960
	ds_read_b128 v[208:211], v142 offset:41984
	ds_read_b128 v[212:215], v142 offset:43008
	ds_read_b128 v[216:219], v142 offset:44032
	global_load_lds_dwordx4 v[220:221], off
	v_lshl_add_u64 v[220:221], v[184:185], 0, s[86:87]
	s_mov_b32 m0, s56
	s_nop 0
	global_load_lds_dwordx4 v[220:221], off
	s_waitcnt vmcnt(8)
	s_waitcnt lgkmcnt(0)
	s_barrier
	s_waitcnt lgkmcnt(0)
	v_mfma_f32_16x16x32_bf16 v[126:129], v[144:147], v[176:179], v[126:129]
	v_mfma_f32_16x16x32_bf16 v[122:125], v[152:155], v[176:179], v[122:125]
	v_mfma_f32_16x16x32_bf16 v[110:113], v[144:147], v[196:199], v[110:113]
	v_mfma_f32_16x16x32_bf16 v[106:109], v[152:155], v[196:199], v[106:109]
	v_mfma_f32_16x16x32_bf16 v[94:97], v[144:147], v[204:207], v[94:97]
	v_mfma_f32_16x16x32_bf16 v[90:93], v[152:155], v[204:207], v[90:93]
	v_mfma_f32_16x16x32_bf16 v[78:81], v[144:147], v[212:215], v[78:81]
	v_mfma_f32_16x16x32_bf16 v[74:77], v[152:155], v[212:215], v[74:77]
	v_mfma_f32_16x16x32_bf16 v[126:129], v[148:151], v[180:183], v[126:129]
	v_mfma_f32_16x16x32_bf16 v[122:125], v[156:159], v[180:183], v[122:125]
	v_mfma_f32_16x16x32_bf16 v[110:113], v[148:151], v[200:203], v[110:113]
	v_mfma_f32_16x16x32_bf16 v[106:109], v[156:159], v[200:203], v[106:109]
	v_mfma_f32_16x16x32_bf16 v[94:97], v[148:151], v[208:211], v[94:97]
	v_mfma_f32_16x16x32_bf16 v[90:93], v[156:159], v[208:211], v[90:93]
	v_mfma_f32_16x16x32_bf16 v[78:81], v[148:151], v[216:219], v[78:81]
	v_mfma_f32_16x16x32_bf16 v[74:77], v[156:159], v[216:219], v[74:77]
	v_mfma_f32_16x16x32_bf16 v[118:121], v[160:163], v[176:179], v[118:121]
	v_mfma_f32_16x16x32_bf16 v[114:117], v[168:171], v[176:179], v[114:117]
	v_mfma_f32_16x16x32_bf16 v[102:105], v[160:163], v[196:199], v[102:105]
	v_mfma_f32_16x16x32_bf16 v[98:101], v[168:171], v[196:199], v[98:101]
	v_mfma_f32_16x16x32_bf16 v[86:89], v[160:163], v[204:207], v[86:89]
	v_mfma_f32_16x16x32_bf16 v[82:85], v[168:171], v[204:207], v[82:85]
	v_mfma_f32_16x16x32_bf16 v[70:73], v[160:163], v[212:215], v[70:73]
	v_mfma_f32_16x16x32_bf16 v[66:69], v[168:171], v[212:215], v[66:69]
	v_mfma_f32_16x16x32_bf16 v[118:121], v[164:167], v[180:183], v[118:121]
	v_mfma_f32_16x16x32_bf16 v[114:117], v[172:175], v[180:183], v[114:117]
	v_mfma_f32_16x16x32_bf16 v[102:105], v[164:167], v[200:203], v[102:105]
	v_mfma_f32_16x16x32_bf16 v[98:101], v[172:175], v[200:203], v[98:101]
	v_mfma_f32_16x16x32_bf16 v[86:89], v[164:167], v[208:211], v[86:89]
	v_mfma_f32_16x16x32_bf16 v[82:85], v[172:175], v[208:211], v[82:85]
	v_mfma_f32_16x16x32_bf16 v[70:73], v[164:167], v[216:219], v[70:73]
	v_mfma_f32_16x16x32_bf16 v[66:69], v[172:175], v[216:219], v[66:69]
	s_barrier
	s_add_i32 s14, s14, s2
	v_lshl_add_u64 v[220:221], v[192:193], 0, s[92:93]
	s_mov_b32 m0, s14
	ds_read_b128 v[176:179], v142 offset:53248
	ds_read_b128 v[180:183], v142 offset:54272
	ds_read_b128 v[196:199], v142 offset:55296
	ds_read_b128 v[200:203], v142 offset:56320
	ds_read_b128 v[204:207], v142 offset:57344
	ds_read_b128 v[208:211], v142 offset:58368
	ds_read_b128 v[212:215], v142 offset:59392
	ds_read_b128 v[216:219], v142 offset:60416
	global_load_lds_dwordx4 v[220:221], off
	v_lshl_add_u64 v[220:221], v[192:193], 0, s[4:5]
	s_add_i32 m0, s14, 0x2000
	s_add_i32 s14, s15, s2
	global_load_lds_dwordx4 v[220:221], off
	v_lshl_add_u64 v[220:221], v[192:193], 0, s[6:7]
	s_mov_b32 m0, s14
	v_lshl_add_u64 v[192:193], v[192:193], 0, s[8:9]
	global_load_lds_dwordx4 v[220:221], off
	s_add_i32 m0, s14, 0x2000
	s_nop 0
	global_load_lds_dwordx4 v[192:193], off
	v_lshl_add_u64 v[192:193], v[184:185], 0, s[92:93]
	s_mov_b32 m0, s59
	v_lshl_add_u64 v[184:185], v[184:185], 0, s[4:5]
	global_load_lds_dwordx4 v[192:193], off
	s_mov_b32 m0, s60
	s_nop 0
	global_load_lds_dwordx4 v[184:185], off
	s_waitcnt vmcnt(8)
	s_waitcnt lgkmcnt(0)
	s_barrier
	s_waitcnt lgkmcnt(0)
	v_mfma_f32_16x16x32_bf16 v[62:65], v[144:147], v[176:179], v[62:65]
	v_mfma_f32_16x16x32_bf16 v[58:61], v[152:155], v[176:179], v[58:61]
	s_add_i32 s43, s43, 2
	v_mfma_f32_16x16x32_bf16 v[46:49], v[144:147], v[196:199], v[46:49]
	s_add_u32 s54, s54, 0x100
	v_mfma_f32_16x16x32_bf16 v[42:45], v[152:155], v[196:199], v[42:45]
	s_addc_u32 s55, s55, 0
	v_mfma_f32_16x16x32_bf16 v[30:33], v[144:147], v[204:207], v[30:33]
	s_add_u32 s14, s52, s54
	v_mfma_f32_16x16x32_bf16 v[26:29], v[152:155], v[204:207], v[26:29]
	s_addc_u32 s15, s53, s55
	v_mfma_f32_16x16x32_bf16 v[14:17], v[144:147], v[212:215], v[14:17]
	s_add_u32 s45, s14, 0x100
	v_mfma_f32_16x16x32_bf16 v[10:13], v[152:155], v[212:215], v[10:13]
	s_addc_u32 s73, s15, 0
	v_mfma_f32_16x16x32_bf16 v[62:65], v[148:151], v[180:183], v[62:65]
	s_add_u32 s74, s24, s54
	v_mfma_f32_16x16x32_bf16 v[58:61], v[156:159], v[180:183], v[58:61]
	s_addc_u32 s75, s25, s55
	v_mfma_f32_16x16x32_bf16 v[46:49], v[148:151], v[200:203], v[46:49]
	s_cmpk_eq_i32 s54, 0x700
	v_mfma_f32_16x16x32_bf16 v[42:45], v[156:159], v[200:203], v[42:45]
	s_cselect_b64 vcc, -1, 0
	v_mfma_f32_16x16x32_bf16 v[30:33], v[148:151], v[208:211], v[30:33]
	s_and_b64 s[14:15], vcc, exec
	v_mfma_f32_16x16x32_bf16 v[26:29], v[156:159], v[208:211], v[26:29]
	s_cselect_b32 s15, s47, s73
	v_mfma_f32_16x16x32_bf16 v[14:17], v[148:151], v[216:219], v[14:17]
	s_cselect_b32 s14, s46, s45
	v_mfma_f32_16x16x32_bf16 v[10:13], v[156:159], v[216:219], v[10:13]
	s_cselect_b32 s75, s49, s75
	v_mfma_f32_16x16x32_bf16 v[54:57], v[160:163], v[176:179], v[54:57]
	s_cselect_b32 s74, s48, s74
	v_mfma_f32_16x16x32_bf16 v[50:53], v[168:171], v[176:179], v[50:53]
	s_add_i32 s45, 0, 0x11000
	v_mfma_f32_16x16x32_bf16 v[38:41], v[160:163], v[196:199], v[38:41]
	s_add_i32 s73, 0, 0x15000
	v_mfma_f32_16x16x32_bf16 v[34:37], v[168:171], v[196:199], v[34:37]
	v_mfma_f32_16x16x32_bf16 v[22:25], v[160:163], v[204:207], v[22:25]
	v_mfma_f32_16x16x32_bf16 v[18:21], v[168:171], v[204:207], v[18:21]
	v_mfma_f32_16x16x32_bf16 v[6:9], v[160:163], v[212:215], v[6:9]
	v_mfma_f32_16x16x32_bf16 v[2:5], v[168:171], v[212:215], v[2:5]
	v_mfma_f32_16x16x32_bf16 v[54:57], v[164:167], v[180:183], v[54:57]
	v_mfma_f32_16x16x32_bf16 v[50:53], v[172:175], v[180:183], v[50:53]
	v_mfma_f32_16x16x32_bf16 v[38:41], v[164:167], v[200:203], v[38:41]
	v_mfma_f32_16x16x32_bf16 v[34:37], v[172:175], v[200:203], v[34:37]
	v_mfma_f32_16x16x32_bf16 v[22:25], v[164:167], v[208:211], v[22:25]
	v_mfma_f32_16x16x32_bf16 v[18:21], v[172:175], v[208:211], v[18:21]
	v_mfma_f32_16x16x32_bf16 v[6:9], v[164:167], v[216:219], v[6:9]
	v_mfma_f32_16x16x32_bf16 v[2:5], v[172:175], v[216:219], v[2:5]
	s_barrier
.LBB0_1111:
	v_add_u32_e32 v131, s45, v1
	ds_read_b128 v[144:147], v131
	ds_read_b128 v[148:151], v131 offset:1024
	ds_read_b128 v[152:155], v131 offset:2048
	ds_read_b128 v[156:159], v131 offset:3072
	v_add_u32_e32 v131, s73, v1
	ds_read_b128 v[160:163], v131
	ds_read_b128 v[164:167], v131 offset:1024
	ds_read_b128 v[168:171], v131 offset:2048
	ds_read_b128 v[172:175], v131 offset:3072
	v_cndmask_b32_e32 v185, v139, v137, vcc
	v_cndmask_b32_e32 v184, v138, v136, vcc
	v_lshl_add_u64 v[192:193], v[140:141], 0, s[54:55]
	v_lshl_add_u64 v[220:221], v[192:193], 0, s[6:7]
	s_add_i32 m0, s29, 0xd000
	ds_read_b128 v[176:179], v142 offset:4096
	ds_read_b128 v[180:183], v142 offset:5120
	ds_read_b128 v[196:199], v142 offset:6144
	ds_read_b128 v[200:203], v142 offset:7168
	ds_read_b128 v[204:207], v142 offset:8192
	ds_read_b128 v[208:211], v142 offset:9216
	ds_read_b128 v[212:215], v142 offset:10240
	ds_read_b128 v[216:219], v142 offset:11264
	global_load_lds_dwordx4 v[220:221], off
	v_lshl_add_u64 v[192:193], v[192:193], 0, s[8:9]
	s_add_i32 m0, s29, 0xf000
	s_nop 0
	global_load_lds_dwordx4 v[192:193], off
	s_waitcnt vmcnt(8)
	s_waitcnt lgkmcnt(0)
	s_barrier
	s_waitcnt lgkmcnt(0)
	v_mfma_f32_16x16x32_bf16 v[126:129], v[144:147], v[176:179], v[126:129]
	v_mfma_f32_16x16x32_bf16 v[122:125], v[152:155], v[176:179], v[122:125]
	v_mfma_f32_16x16x32_bf16 v[110:113], v[144:147], v[196:199], v[110:113]
	v_mfma_f32_16x16x32_bf16 v[106:109], v[152:155], v[196:199], v[106:109]
	v_mfma_f32_16x16x32_bf16 v[94:97], v[144:147], v[204:207], v[94:97]
	v_mfma_f32_16x16x32_bf16 v[90:93], v[152:155], v[204:207], v[90:93]
	v_mfma_f32_16x16x32_bf16 v[78:81], v[144:147], v[212:215], v[78:81]
	v_mfma_f32_16x16x32_bf16 v[74:77], v[152:155], v[212:215], v[74:77]
	v_mfma_f32_16x16x32_bf16 v[126:129], v[148:151], v[180:183], v[126:129]
	v_mfma_f32_16x16x32_bf16 v[122:125], v[156:159], v[180:183], v[122:125]
	v_mfma_f32_16x16x32_bf16 v[110:113], v[148:151], v[200:203], v[110:113]
	v_mfma_f32_16x16x32_bf16 v[106:109], v[156:159], v[200:203], v[106:109]
	v_mfma_f32_16x16x32_bf16 v[94:97], v[148:151], v[208:211], v[94:97]
	v_mfma_f32_16x16x32_bf16 v[90:93], v[156:159], v[208:211], v[90:93]
	v_mfma_f32_16x16x32_bf16 v[78:81], v[148:151], v[216:219], v[78:81]
	v_mfma_f32_16x16x32_bf16 v[74:77], v[156:159], v[216:219], v[74:77]
	v_mfma_f32_16x16x32_bf16 v[118:121], v[160:163], v[176:179], v[118:121]
	v_mfma_f32_16x16x32_bf16 v[114:117], v[168:171], v[176:179], v[114:117]
	v_mfma_f32_16x16x32_bf16 v[102:105], v[160:163], v[196:199], v[102:105]
	v_mfma_f32_16x16x32_bf16 v[98:101], v[168:171], v[196:199], v[98:101]
	v_mfma_f32_16x16x32_bf16 v[86:89], v[160:163], v[204:207], v[86:89]
	v_mfma_f32_16x16x32_bf16 v[82:85], v[168:171], v[204:207], v[82:85]
	v_mfma_f32_16x16x32_bf16 v[70:73], v[160:163], v[212:215], v[70:73]
	v_mfma_f32_16x16x32_bf16 v[66:69], v[168:171], v[212:215], v[66:69]
	v_mfma_f32_16x16x32_bf16 v[118:121], v[164:167], v[180:183], v[118:121]
	v_mfma_f32_16x16x32_bf16 v[114:117], v[172:175], v[180:183], v[114:117]
	v_mfma_f32_16x16x32_bf16 v[102:105], v[164:167], v[200:203], v[102:105]
	v_mfma_f32_16x16x32_bf16 v[98:101], v[172:175], v[200:203], v[98:101]
	v_mfma_f32_16x16x32_bf16 v[86:89], v[164:167], v[208:211], v[86:89]
	v_mfma_f32_16x16x32_bf16 v[82:85], v[172:175], v[208:211], v[82:85]
	v_mfma_f32_16x16x32_bf16 v[70:73], v[164:167], v[216:219], v[70:73]
	v_mfma_f32_16x16x32_bf16 v[66:69], v[172:175], v[216:219], v[66:69]
	s_barrier
	s_add_i32 s45, s45, s2
	v_lshl_add_u64 v[192:193], s[74:75], 0, v[186:187]
	s_mov_b32 m0, s45
	ds_read_b128 v[176:179], v142 offset:20480
	ds_read_b128 v[180:183], v142 offset:21504
	ds_read_b128 v[196:199], v142 offset:22528
	ds_read_b128 v[200:203], v142 offset:23552
	ds_read_b128 v[204:207], v142 offset:24576
	ds_read_b128 v[208:211], v142 offset:25600
	ds_read_b128 v[212:215], v142 offset:26624
	ds_read_b128 v[216:219], v142 offset:27648
	global_load_lds_dwordx4 v186, s[74:75]
	v_lshl_add_u64 v[220:221], v[192:193], 0, s[82:83]
	s_add_i32 m0, s45, 0x2000
	s_add_i32 s45, s73, s2
	global_load_lds_dwordx4 v[220:221], off
	v_lshl_add_u64 v[220:221], v[192:193], 0, s[64:65]
	s_mov_b32 m0, s45
	v_lshl_add_u64 v[184:185], s[14:15], 0, v[184:185]
	global_load_lds_dwordx4 v[220:221], off
	v_lshl_add_u64 v[220:221], v[192:193], 0, s[86:87]
	s_add_i32 m0, s45, 0x2000
	s_nop 0
	global_load_lds_dwordx4 v[220:221], off
	s_mov_b32 m0, s33
	v_lshl_add_u64 v[220:221], v[184:185], 0, s[82:83]
	global_load_lds_dwordx4 v[184:185], off
	s_mov_b32 m0, s34
	s_nop 0
	global_load_lds_dwordx4 v[220:221], off
	s_waitcnt vmcnt(8)
	s_waitcnt lgkmcnt(0)
	s_barrier
	s_waitcnt lgkmcnt(0)
	v_mfma_f32_16x16x32_bf16 v[62:65], v[144:147], v[176:179], v[62:65]
	v_mfma_f32_16x16x32_bf16 v[58:61], v[152:155], v[176:179], v[58:61]
	v_mfma_f32_16x16x32_bf16 v[46:49], v[144:147], v[196:199], v[46:49]
	v_mfma_f32_16x16x32_bf16 v[42:45], v[152:155], v[196:199], v[42:45]
	v_mfma_f32_16x16x32_bf16 v[30:33], v[144:147], v[204:207], v[30:33]
	v_mfma_f32_16x16x32_bf16 v[26:29], v[152:155], v[204:207], v[26:29]
	v_mfma_f32_16x16x32_bf16 v[14:17], v[144:147], v[212:215], v[14:17]
	v_mfma_f32_16x16x32_bf16 v[10:13], v[152:155], v[212:215], v[10:13]
	v_mfma_f32_16x16x32_bf16 v[62:65], v[148:151], v[180:183], v[62:65]
	v_mfma_f32_16x16x32_bf16 v[58:61], v[156:159], v[180:183], v[58:61]
	v_mfma_f32_16x16x32_bf16 v[46:49], v[148:151], v[200:203], v[46:49]
	v_mfma_f32_16x16x32_bf16 v[42:45], v[156:159], v[200:203], v[42:45]
	v_mfma_f32_16x16x32_bf16 v[30:33], v[148:151], v[208:211], v[30:33]
	v_mfma_f32_16x16x32_bf16 v[26:29], v[156:159], v[208:211], v[26:29]
	v_mfma_f32_16x16x32_bf16 v[14:17], v[148:151], v[216:219], v[14:17]
	v_mfma_f32_16x16x32_bf16 v[10:13], v[156:159], v[216:219], v[10:13]
	v_mfma_f32_16x16x32_bf16 v[54:57], v[160:163], v[176:179], v[54:57]
	v_mfma_f32_16x16x32_bf16 v[50:53], v[168:171], v[176:179], v[50:53]
	v_mfma_f32_16x16x32_bf16 v[38:41], v[160:163], v[196:199], v[38:41]
	v_mfma_f32_16x16x32_bf16 v[34:37], v[168:171], v[196:199], v[34:37]
	v_mfma_f32_16x16x32_bf16 v[22:25], v[160:163], v[204:207], v[22:25]
	v_mfma_f32_16x16x32_bf16 v[18:21], v[168:171], v[204:207], v[18:21]
	v_mfma_f32_16x16x32_bf16 v[6:9], v[160:163], v[212:215], v[6:9]
	v_mfma_f32_16x16x32_bf16 v[2:5], v[168:171], v[212:215], v[2:5]
	v_mfma_f32_16x16x32_bf16 v[54:57], v[164:167], v[180:183], v[54:57]
	v_mfma_f32_16x16x32_bf16 v[50:53], v[172:175], v[180:183], v[50:53]
	v_mfma_f32_16x16x32_bf16 v[38:41], v[164:167], v[200:203], v[38:41]
	v_mfma_f32_16x16x32_bf16 v[34:37], v[172:175], v[200:203], v[34:37]
	v_mfma_f32_16x16x32_bf16 v[22:25], v[164:167], v[208:211], v[22:25]
	v_mfma_f32_16x16x32_bf16 v[18:21], v[172:175], v[208:211], v[18:21]
	v_mfma_f32_16x16x32_bf16 v[6:9], v[164:167], v[216:219], v[6:9]
	v_mfma_f32_16x16x32_bf16 v[2:5], v[172:175], v[216:219], v[2:5]
	s_barrier
	s_add_i32 s14, 0, 0x19000
	v_add_u32_e32 v131, s14, v1
	s_add_i32 s15, 0, 0x1d000
	ds_read_b128 v[144:147], v131
	ds_read_b128 v[148:151], v131 offset:1024
	ds_read_b128 v[152:155], v131 offset:2048
	ds_read_b128 v[156:159], v131 offset:3072
	v_add_u32_e32 v131, s15, v1
	ds_read_b128 v[160:163], v131
	ds_read_b128 v[164:167], v131 offset:1024
	ds_read_b128 v[168:171], v131 offset:2048
	ds_read_b128 v[172:175], v131 offset:3072
	s_mov_b32 m0, s35
	v_lshl_add_u64 v[220:221], v[184:185], 0, s[64:65]
	ds_read_b128 v[176:179], v142 offset:36864
	ds_read_b128 v[180:183], v142 offset:37888
	ds_read_b128 v[196:199], v142 offset:38912
	ds_read_b128 v[200:203], v142 offset:39936
	ds_read_b128 v[204:207], v142 offset:40960
	ds_read_b128 v[208:211], v142 offset:41984
	ds_read_b128 v[212:215], v142 offset:43008
	ds_read_b128 v[216:219], v142 offset:44032
	global_load_lds_dwordx4 v[220:221], off
	v_lshl_add_u64 v[220:221], v[184:185], 0, s[86:87]
	s_mov_b32 m0, s56
	s_nop 0
	global_load_lds_dwordx4 v[220:221], off
	s_waitcnt vmcnt(8)
	s_waitcnt lgkmcnt(0)
	s_barrier
	s_waitcnt lgkmcnt(0)
	v_mfma_f32_16x16x32_bf16 v[126:129], v[144:147], v[176:179], v[126:129]
	v_mfma_f32_16x16x32_bf16 v[122:125], v[152:155], v[176:179], v[122:125]
	v_mfma_f32_16x16x32_bf16 v[110:113], v[144:147], v[196:199], v[110:113]
	v_mfma_f32_16x16x32_bf16 v[106:109], v[152:155], v[196:199], v[106:109]
	v_mfma_f32_16x16x32_bf16 v[94:97], v[144:147], v[204:207], v[94:97]
	v_mfma_f32_16x16x32_bf16 v[90:93], v[152:155], v[204:207], v[90:93]
	v_mfma_f32_16x16x32_bf16 v[78:81], v[144:147], v[212:215], v[78:81]
	v_mfma_f32_16x16x32_bf16 v[74:77], v[152:155], v[212:215], v[74:77]
	v_mfma_f32_16x16x32_bf16 v[126:129], v[148:151], v[180:183], v[126:129]
	v_mfma_f32_16x16x32_bf16 v[122:125], v[156:159], v[180:183], v[122:125]
	v_mfma_f32_16x16x32_bf16 v[110:113], v[148:151], v[200:203], v[110:113]
	v_mfma_f32_16x16x32_bf16 v[106:109], v[156:159], v[200:203], v[106:109]
	v_mfma_f32_16x16x32_bf16 v[94:97], v[148:151], v[208:211], v[94:97]
	v_mfma_f32_16x16x32_bf16 v[90:93], v[156:159], v[208:211], v[90:93]
	v_mfma_f32_16x16x32_bf16 v[78:81], v[148:151], v[216:219], v[78:81]
	v_mfma_f32_16x16x32_bf16 v[74:77], v[156:159], v[216:219], v[74:77]
	v_mfma_f32_16x16x32_bf16 v[118:121], v[160:163], v[176:179], v[118:121]
	v_mfma_f32_16x16x32_bf16 v[114:117], v[168:171], v[176:179], v[114:117]
	v_mfma_f32_16x16x32_bf16 v[102:105], v[160:163], v[196:199], v[102:105]
	v_mfma_f32_16x16x32_bf16 v[98:101], v[168:171], v[196:199], v[98:101]
	v_mfma_f32_16x16x32_bf16 v[86:89], v[160:163], v[204:207], v[86:89]
	v_mfma_f32_16x16x32_bf16 v[82:85], v[168:171], v[204:207], v[82:85]
	v_mfma_f32_16x16x32_bf16 v[70:73], v[160:163], v[212:215], v[70:73]
	v_mfma_f32_16x16x32_bf16 v[66:69], v[168:171], v[212:215], v[66:69]
	v_mfma_f32_16x16x32_bf16 v[118:121], v[164:167], v[180:183], v[118:121]
	v_mfma_f32_16x16x32_bf16 v[114:117], v[172:175], v[180:183], v[114:117]
	v_mfma_f32_16x16x32_bf16 v[102:105], v[164:167], v[200:203], v[102:105]
	v_mfma_f32_16x16x32_bf16 v[98:101], v[172:175], v[200:203], v[98:101]
	v_mfma_f32_16x16x32_bf16 v[86:89], v[164:167], v[208:211], v[86:89]
	v_mfma_f32_16x16x32_bf16 v[82:85], v[172:175], v[208:211], v[82:85]
	v_mfma_f32_16x16x32_bf16 v[70:73], v[164:167], v[216:219], v[70:73]
	v_mfma_f32_16x16x32_bf16 v[66:69], v[172:175], v[216:219], v[66:69]
	s_barrier
	s_add_i32 s14, s14, s2
	v_lshl_add_u64 v[220:221], v[192:193], 0, s[92:93]
	s_mov_b32 m0, s14
	ds_read_b128 v[176:179], v142 offset:53248
	ds_read_b128 v[180:183], v142 offset:54272
	ds_read_b128 v[196:199], v142 offset:55296
	ds_read_b128 v[200:203], v142 offset:56320
	ds_read_b128 v[204:207], v142 offset:57344
	ds_read_b128 v[208:211], v142 offset:58368
	ds_read_b128 v[212:215], v142 offset:59392
	ds_read_b128 v[216:219], v142 offset:60416
	global_load_lds_dwordx4 v[220:221], off
	v_lshl_add_u64 v[220:221], v[192:193], 0, s[4:5]
	s_add_i32 m0, s14, 0x2000
	s_add_i32 s14, s15, s2
	global_load_lds_dwordx4 v[220:221], off
	v_lshl_add_u64 v[220:221], v[192:193], 0, s[6:7]
	s_mov_b32 m0, s14
	v_lshl_add_u64 v[192:193], v[192:193], 0, s[8:9]
	global_load_lds_dwordx4 v[220:221], off
	s_add_i32 m0, s14, 0x2000
	s_nop 0
	global_load_lds_dwordx4 v[192:193], off
	v_lshl_add_u64 v[192:193], v[184:185], 0, s[92:93]
	s_mov_b32 m0, s59
	v_lshl_add_u64 v[184:185], v[184:185], 0, s[4:5]
	global_load_lds_dwordx4 v[192:193], off
	s_mov_b32 m0, s60
	s_nop 0
	global_load_lds_dwordx4 v[184:185], off
	s_waitcnt vmcnt(8)
	s_waitcnt lgkmcnt(0)
	s_barrier
	s_waitcnt lgkmcnt(0)
	v_mfma_f32_16x16x32_bf16 v[62:65], v[144:147], v[176:179], v[62:65]
	v_mfma_f32_16x16x32_bf16 v[58:61], v[152:155], v[176:179], v[58:61]
	s_add_i32 s43, s43, 2
	v_mfma_f32_16x16x32_bf16 v[46:49], v[144:147], v[196:199], v[46:49]
	s_add_u32 s54, s54, 0x100
	v_mfma_f32_16x16x32_bf16 v[42:45], v[152:155], v[196:199], v[42:45]
	s_addc_u32 s55, s55, 0
	v_mfma_f32_16x16x32_bf16 v[30:33], v[144:147], v[204:207], v[30:33]
	s_add_u32 s14, s52, s54
	v_mfma_f32_16x16x32_bf16 v[26:29], v[152:155], v[204:207], v[26:29]
	s_addc_u32 s15, s53, s55
	v_mfma_f32_16x16x32_bf16 v[14:17], v[144:147], v[212:215], v[14:17]
	s_add_u32 s45, s14, 0x100
	v_mfma_f32_16x16x32_bf16 v[10:13], v[152:155], v[212:215], v[10:13]
	s_addc_u32 s73, s15, 0
	v_mfma_f32_16x16x32_bf16 v[62:65], v[148:151], v[180:183], v[62:65]
	s_add_u32 s74, s24, s54
	v_mfma_f32_16x16x32_bf16 v[58:61], v[156:159], v[180:183], v[58:61]
	s_addc_u32 s75, s25, s55
	v_mfma_f32_16x16x32_bf16 v[46:49], v[148:151], v[200:203], v[46:49]
	s_cmpk_eq_i32 s54, 0x700
	v_mfma_f32_16x16x32_bf16 v[42:45], v[156:159], v[200:203], v[42:45]
	s_cselect_b64 vcc, -1, 0
	v_mfma_f32_16x16x32_bf16 v[30:33], v[148:151], v[208:211], v[30:33]
	s_and_b64 s[14:15], vcc, exec
	v_mfma_f32_16x16x32_bf16 v[26:29], v[156:159], v[208:211], v[26:29]
	s_cselect_b32 s15, s47, s73
	v_mfma_f32_16x16x32_bf16 v[14:17], v[148:151], v[216:219], v[14:17]
	s_cselect_b32 s14, s46, s45
	v_mfma_f32_16x16x32_bf16 v[10:13], v[156:159], v[216:219], v[10:13]
	s_cselect_b32 s75, s49, s75
	v_mfma_f32_16x16x32_bf16 v[54:57], v[160:163], v[176:179], v[54:57]
	s_cselect_b32 s74, s48, s74
	v_mfma_f32_16x16x32_bf16 v[50:53], v[168:171], v[176:179], v[50:53]
	s_add_i32 s45, 0, 0x11000
	v_mfma_f32_16x16x32_bf16 v[38:41], v[160:163], v[196:199], v[38:41]
	s_add_i32 s73, 0, 0x15000
	v_mfma_f32_16x16x32_bf16 v[34:37], v[168:171], v[196:199], v[34:37]
	v_mfma_f32_16x16x32_bf16 v[22:25], v[160:163], v[204:207], v[22:25]
	v_mfma_f32_16x16x32_bf16 v[18:21], v[168:171], v[204:207], v[18:21]
	v_mfma_f32_16x16x32_bf16 v[6:9], v[160:163], v[212:215], v[6:9]
	v_mfma_f32_16x16x32_bf16 v[2:5], v[168:171], v[212:215], v[2:5]
	v_mfma_f32_16x16x32_bf16 v[54:57], v[164:167], v[180:183], v[54:57]
	v_mfma_f32_16x16x32_bf16 v[50:53], v[172:175], v[180:183], v[50:53]
	v_mfma_f32_16x16x32_bf16 v[38:41], v[164:167], v[200:203], v[38:41]
	v_mfma_f32_16x16x32_bf16 v[34:37], v[172:175], v[200:203], v[34:37]
	v_mfma_f32_16x16x32_bf16 v[22:25], v[164:167], v[208:211], v[22:25]
	v_mfma_f32_16x16x32_bf16 v[18:21], v[172:175], v[208:211], v[18:21]
	v_mfma_f32_16x16x32_bf16 v[6:9], v[164:167], v[216:219], v[6:9]
	v_mfma_f32_16x16x32_bf16 v[2:5], v[172:175], v[216:219], v[2:5]
	s_barrier
	s_cmp_gt_u32 s43, 13
	s_cbranch_scc0 .LBB0_1111
	s_and_b64 vcc, exec, s[0:1]
	s_cbranch_vccnz .Lepi1_out
	s_setprio 1
	s_branch .Lepid_out

.Lepid_out:
	s_and_b64 vcc, exec, s[40:41]
	s_cbranch_vccz .LBB0_1114
	s_barrier

.Lprio_up:
	s_setprio 0
.Lpriod_up:
	s_add_u32 s1, s72, 0x100
	s_addc_u32 s2, s73, 0
	s_add_u32 s14, s70, 0x80
	v_mov_b32_e32 v59, v187
	v_mov_b32_e32 v65, v187
	s_addc_u32 s15, s71, 0
	v_lshl_add_u64 v[74:75], s[14:15], 0, v[64:65]
	v_lshl_add_u64 v[76:77], s[14:15], 0, v[58:59]
	s_mov_b32 s34, -2
	s_mov_b64 s[40:41], 0
	s_add_u32 s14, s70, s40
	s_addc_u32 s15, s71, s41
	s_add_u32 s35, s14, 0x100
	s_addc_u32 s55, s15, 0
	s_add_u32 s61, s1, s40
	s_addc_u32 s69, s2, s41
	s_cmpk_eq_i32 s40, 0x700
	s_cselect_b64 vcc, -1, 0
	s_and_b64 s[14:15], vcc, exec
	s_cselect_b32 s15, s59, s55
	s_cselect_b32 s14, s58, s35
	s_cselect_b32 s73, s57, s69
	s_cselect_b32 s72, s56, s61
	s_add_i32 s35, 0, 0x11000
	v_add_u32_e32 v63, s35, v165
	s_add_i32 s55, 0, 0x15000
	ds_read_b128 v[78:81], v63
	ds_read_b128 v[154:157], v63 offset:1024
	ds_read_b128 v[158:161], v63 offset:2048
	ds_read_b128 v[172:175], v63 offset:3072
	v_add_u32_e32 v63, s55, v165
	ds_read_b128 v[176:179], v63
	ds_read_b128 v[180:183], v63 offset:1024
	ds_read_b128 v[196:199], v63 offset:2048
	ds_read_b128 v[200:203], v63 offset:3072
	v_cndmask_b32_e32 v186, v62, v171, vcc
	v_cndmask_b32_e32 v184, v60, v170, vcc
	v_cndmask_b32_e32 v59, v58, v168, vcc
	v_cndmask_b32_e32 v61, v64, v169, vcc
	v_lshl_add_u64 v[192:193], v[76:77], 0, s[40:41]
	s_add_i32 m0, s24, 0xd000
	ds_read_b128 v[204:207], v166 offset:4096
	ds_read_b128 v[208:211], v166 offset:5120
	ds_read_b128 v[212:215], v166 offset:6144
	ds_read_b128 v[216:219], v166 offset:7168
	ds_read_b128 v[220:223], v166 offset:8192
	ds_read_b128 v[240:243], v166 offset:9216
	ds_read_b128 v[244:247], v166 offset:10240
	ds_read_b128 v[248:251], v166 offset:11264
	global_load_lds_dwordx4 v[192:193], off
	v_lshl_add_u64 v[192:193], v[74:75], 0, s[40:41]
	s_add_i32 m0, s24, 0xf000
	s_nop 0
	global_load_lds_dwordx4 v[192:193], off
	s_waitcnt vmcnt(8)
	s_waitcnt lgkmcnt(0)
	s_barrier
	s_waitcnt lgkmcnt(0)
	v_mfma_f32_16x16x32_bf16 v[142:145], v[78:81], v[204:207], 0
	v_mfma_f32_16x16x32_bf16 v[134:137], v[158:161], v[204:207], 0
	v_mfma_f32_16x16x32_bf16 v[126:129], v[78:81], v[212:215], 0
	v_mfma_f32_16x16x32_bf16 v[118:121], v[158:161], v[212:215], 0
	v_mfma_f32_16x16x32_bf16 v[110:113], v[78:81], v[220:223], 0
	v_mfma_f32_16x16x32_bf16 v[102:105], v[158:161], v[220:223], 0
	v_mfma_f32_16x16x32_bf16 v[94:97], v[78:81], v[244:247], 0
	v_mfma_f32_16x16x32_bf16 v[86:89], v[158:161], v[244:247], 0
	v_mfma_f32_16x16x32_bf16 v[142:145], v[154:157], v[208:211], v[142:145]
	v_mfma_f32_16x16x32_bf16 v[134:137], v[172:175], v[208:211], v[134:137]
	v_mfma_f32_16x16x32_bf16 v[126:129], v[154:157], v[216:219], v[126:129]
	v_mfma_f32_16x16x32_bf16 v[118:121], v[172:175], v[216:219], v[118:121]
	v_mfma_f32_16x16x32_bf16 v[110:113], v[154:157], v[240:243], v[110:113]
	v_mfma_f32_16x16x32_bf16 v[102:105], v[172:175], v[240:243], v[102:105]
	v_mfma_f32_16x16x32_bf16 v[94:97], v[154:157], v[248:251], v[94:97]
	v_mfma_f32_16x16x32_bf16 v[86:89], v[172:175], v[248:251], v[86:89]
	v_mfma_f32_16x16x32_bf16 v[138:141], v[176:179], v[204:207], 0
	v_mfma_f32_16x16x32_bf16 v[130:133], v[196:199], v[204:207], 0
	v_mfma_f32_16x16x32_bf16 v[122:125], v[176:179], v[212:215], 0
	v_mfma_f32_16x16x32_bf16 v[114:117], v[196:199], v[212:215], 0
	v_mfma_f32_16x16x32_bf16 v[106:109], v[176:179], v[220:223], 0
	v_mfma_f32_16x16x32_bf16 v[98:101], v[196:199], v[220:223], 0
	v_mfma_f32_16x16x32_bf16 v[90:93], v[176:179], v[244:247], 0
	v_mfma_f32_16x16x32_bf16 v[82:85], v[196:199], v[244:247], 0
	v_mfma_f32_16x16x32_bf16 v[138:141], v[180:183], v[208:211], v[138:141]
	v_mfma_f32_16x16x32_bf16 v[130:133], v[200:203], v[208:211], v[130:133]
	v_mfma_f32_16x16x32_bf16 v[122:125], v[180:183], v[216:219], v[122:125]
	v_mfma_f32_16x16x32_bf16 v[114:117], v[200:203], v[216:219], v[114:117]
	v_mfma_f32_16x16x32_bf16 v[106:109], v[180:183], v[240:243], v[106:109]
	v_mfma_f32_16x16x32_bf16 v[98:101], v[200:203], v[240:243], v[98:101]
	v_mfma_f32_16x16x32_bf16 v[90:93], v[180:183], v[248:251], v[90:93]
	v_mfma_f32_16x16x32_bf16 v[82:85], v[200:203], v[248:251], v[82:85]
	s_barrier
	s_add_i32 s35, s35, s17
	v_lshl_add_u64 v[192:193], s[72:73], 0, v[148:149]
	s_mov_b32 m0, s35
	ds_read_b128 v[204:207], v166 offset:20480
	ds_read_b128 v[208:211], v166 offset:21504
	ds_read_b128 v[212:215], v166 offset:22528
	ds_read_b128 v[216:219], v166 offset:23552
	ds_read_b128 v[220:223], v166 offset:24576
	ds_read_b128 v[240:243], v166 offset:25600
	ds_read_b128 v[244:247], v166 offset:26624
	ds_read_b128 v[248:251], v166 offset:27648
	global_load_lds_dwordx4 v[192:193], off
	v_lshl_add_u64 v[224:225], v[192:193], 0, s[82:83]
	s_add_i32 m0, s35, 0x2000
	s_add_i32 s35, s55, s17
	global_load_lds_dwordx4 v[224:225], off
	v_lshl_add_u64 v[224:225], v[192:193], 0, s[64:65]
	s_mov_b32 m0, s35
	v_mov_b32_e32 v185, v187
	global_load_lds_dwordx4 v[224:225], off
	v_lshl_add_u64 v[224:225], v[192:193], 0, s[86:87]
	s_add_i32 m0, s35, 0x2000
	s_nop 0
	global_load_lds_dwordx4 v[224:225], off
	s_mov_b32 m0, s25
	v_lshl_add_u64 v[224:225], s[14:15], 0, v[186:187]
	global_load_lds_dwordx4 v186, s[14:15]
	s_mov_b32 m0, s28
	s_nop 0
	global_load_lds_dwordx4 v184, s[14:15]
	s_waitcnt vmcnt(8)
	s_waitcnt lgkmcnt(0)
	v_lshl_add_u64 v[184:185], s[14:15], 0, v[184:185]
	s_barrier
	s_cmp_lg_u64 s[38:39], 0
	s_cbranch_scc1 .Lup_tokskip
	v_lshlrev_b32_e32 v2, 10, v2
	v_lshlrev_b32_e32 v3, 10, v3
	v_lshlrev_b32_e32 v5, 10, v5
	v_lshlrev_b32_e32 v4, 10, v4
	v_add_lshl_u32 v168, v5, v164, 1
	v_add_lshl_u32 v170, v3, v164, 1
	v_add_lshl_u32 v171, v2, v164, 1
	v_add_lshl_u32 v169, v4, v164, 1

.LBB0_1339:
	v_add_u32_e32 v63, s35, v165
	ds_read_b128 v[78:81], v63
	ds_read_b128 v[154:157], v63 offset:1024
	ds_read_b128 v[158:161], v63 offset:2048
	ds_read_b128 v[172:175], v63 offset:3072
	v_add_u32_e32 v63, s55, v165
	ds_read_b128 v[176:179], v63
	ds_read_b128 v[180:183], v63 offset:1024
	ds_read_b128 v[196:199], v63 offset:2048
	ds_read_b128 v[200:203], v63 offset:3072
	v_cndmask_b32_e32 v186, v62, v171, vcc
	v_cndmask_b32_e32 v184, v60, v170, vcc
	v_cndmask_b32_e32 v59, v58, v168, vcc
	v_cndmask_b32_e32 v61, v64, v169, vcc
	v_lshl_add_u64 v[192:193], v[76:77], 0, s[40:41]
	s_add_i32 m0, s24, 0xd000
	ds_read_b128 v[204:207], v166 offset:4096
	ds_read_b128 v[208:211], v166 offset:5120
	ds_read_b128 v[212:215], v166 offset:6144
	ds_read_b128 v[216:219], v166 offset:7168
	ds_read_b128 v[220:223], v166 offset:8192
	ds_read_b128 v[240:243], v166 offset:9216
	ds_read_b128 v[244:247], v166 offset:10240
	ds_read_b128 v[248:251], v166 offset:11264
	global_load_lds_dwordx4 v[192:193], off
	v_lshl_add_u64 v[192:193], v[74:75], 0, s[40:41]
	s_add_i32 m0, s24, 0xf000
	s_nop 0
	global_load_lds_dwordx4 v[192:193], off
	s_waitcnt vmcnt(8)
	s_waitcnt lgkmcnt(0)
	s_barrier
	s_waitcnt lgkmcnt(0)
	v_mfma_f32_16x16x32_bf16 v[142:145], v[78:81], v[204:207], v[142:145]
	v_mfma_f32_16x16x32_bf16 v[134:137], v[158:161], v[204:207], v[134:137]
	v_mfma_f32_16x16x32_bf16 v[126:129], v[78:81], v[212:215], v[126:129]
	v_mfma_f32_16x16x32_bf16 v[118:121], v[158:161], v[212:215], v[118:121]
	v_mfma_f32_16x16x32_bf16 v[110:113], v[78:81], v[220:223], v[110:113]
	v_mfma_f32_16x16x32_bf16 v[102:105], v[158:161], v[220:223], v[102:105]
	v_mfma_f32_16x16x32_bf16 v[94:97], v[78:81], v[244:247], v[94:97]
	v_mfma_f32_16x16x32_bf16 v[86:89], v[158:161], v[244:247], v[86:89]
	v_mfma_f32_16x16x32_bf16 v[142:145], v[154:157], v[208:211], v[142:145]
	v_mfma_f32_16x16x32_bf16 v[134:137], v[172:175], v[208:211], v[134:137]
	v_mfma_f32_16x16x32_bf16 v[126:129], v[154:157], v[216:219], v[126:129]
	v_mfma_f32_16x16x32_bf16 v[118:121], v[172:175], v[216:219], v[118:121]
	v_mfma_f32_16x16x32_bf16 v[110:113], v[154:157], v[240:243], v[110:113]
	v_mfma_f32_16x16x32_bf16 v[102:105], v[172:175], v[240:243], v[102:105]
	v_mfma_f32_16x16x32_bf16 v[94:97], v[154:157], v[248:251], v[94:97]
	v_mfma_f32_16x16x32_bf16 v[86:89], v[172:175], v[248:251], v[86:89]
	v_mfma_f32_16x16x32_bf16 v[138:141], v[176:179], v[204:207], v[138:141]
	v_mfma_f32_16x16x32_bf16 v[130:133], v[196:199], v[204:207], v[130:133]
	v_mfma_f32_16x16x32_bf16 v[122:125], v[176:179], v[212:215], v[122:125]
	v_mfma_f32_16x16x32_bf16 v[114:117], v[196:199], v[212:215], v[114:117]
	v_mfma_f32_16x16x32_bf16 v[106:109], v[176:179], v[220:223], v[106:109]
	v_mfma_f32_16x16x32_bf16 v[98:101], v[196:199], v[220:223], v[98:101]
	v_mfma_f32_16x16x32_bf16 v[90:93], v[176:179], v[244:247], v[90:93]
	v_mfma_f32_16x16x32_bf16 v[82:85], v[196:199], v[244:247], v[82:85]
	v_mfma_f32_16x16x32_bf16 v[138:141], v[180:183], v[208:211], v[138:141]
	v_mfma_f32_16x16x32_bf16 v[130:133], v[200:203], v[208:211], v[130:133]
	v_mfma_f32_16x16x32_bf16 v[122:125], v[180:183], v[216:219], v[122:125]
	v_mfma_f32_16x16x32_bf16 v[114:117], v[200:203], v[216:219], v[114:117]
	v_mfma_f32_16x16x32_bf16 v[106:109], v[180:183], v[240:243], v[106:109]
	v_mfma_f32_16x16x32_bf16 v[98:101], v[200:203], v[240:243], v[98:101]
	v_mfma_f32_16x16x32_bf16 v[90:93], v[180:183], v[248:251], v[90:93]
	v_mfma_f32_16x16x32_bf16 v[82:85], v[200:203], v[248:251], v[82:85]
	s_barrier
	s_add_i32 s35, s35, s17
	v_lshl_add_u64 v[192:193], s[72:73], 0, v[148:149]
	s_mov_b32 m0, s35
	ds_read_b128 v[204:207], v166 offset:20480
	ds_read_b128 v[208:211], v166 offset:21504
	ds_read_b128 v[212:215], v166 offset:22528
	ds_read_b128 v[216:219], v166 offset:23552
	ds_read_b128 v[220:223], v166 offset:24576
	ds_read_b128 v[240:243], v166 offset:25600
	ds_read_b128 v[244:247], v166 offset:26624
	ds_read_b128 v[248:251], v166 offset:27648
	global_load_lds_dwordx4 v[192:193], off
	v_lshl_add_u64 v[224:225], v[192:193], 0, s[82:83]
	s_add_i32 m0, s35, 0x2000
	s_add_i32 s35, s55, s17
	global_load_lds_dwordx4 v[224:225], off
	v_lshl_add_u64 v[224:225], v[192:193], 0, s[64:65]
	s_mov_b32 m0, s35
	v_mov_b32_e32 v185, v187
	global_load_lds_dwordx4 v[224:225], off
	v_lshl_add_u64 v[224:225], v[192:193], 0, s[86:87]
	s_add_i32 m0, s35, 0x2000
	s_nop 0
	global_load_lds_dwordx4 v[224:225], off
	s_mov_b32 m0, s25
	v_lshl_add_u64 v[224:225], s[14:15], 0, v[186:187]
	global_load_lds_dwordx4 v186, s[14:15]
	s_mov_b32 m0, s28
	s_nop 0
	global_load_lds_dwordx4 v184, s[14:15]
	s_waitcnt vmcnt(8)
	s_waitcnt lgkmcnt(0)
	v_lshl_add_u64 v[184:185], s[14:15], 0, v[184:185]
	s_barrier
	s_waitcnt lgkmcnt(0)
	v_mfma_f32_16x16x32_bf16 v[70:73], v[78:81], v[204:207], v[70:73]
	v_mfma_f32_16x16x32_bf16 v[54:57], v[158:161], v[204:207], v[54:57]
	v_mfma_f32_16x16x32_bf16 v[46:49], v[78:81], v[212:215], v[46:49]
	v_mfma_f32_16x16x32_bf16 v[38:41], v[158:161], v[212:215], v[38:41]
	v_mfma_f32_16x16x32_bf16 v[30:33], v[78:81], v[220:223], v[30:33]
	v_mfma_f32_16x16x32_bf16 v[22:25], v[158:161], v[220:223], v[22:25]
	v_mfma_f32_16x16x32_bf16 v[14:17], v[78:81], v[244:247], v[14:17]
	v_mfma_f32_16x16x32_bf16 v[6:9], v[158:161], v[244:247], v[6:9]
	v_mfma_f32_16x16x32_bf16 v[70:73], v[154:157], v[208:211], v[70:73]
	v_mfma_f32_16x16x32_bf16 v[54:57], v[172:175], v[208:211], v[54:57]
	v_mfma_f32_16x16x32_bf16 v[46:49], v[154:157], v[216:219], v[46:49]
	v_mfma_f32_16x16x32_bf16 v[38:41], v[172:175], v[216:219], v[38:41]
	v_mfma_f32_16x16x32_bf16 v[30:33], v[154:157], v[240:243], v[30:33]
	v_mfma_f32_16x16x32_bf16 v[22:25], v[172:175], v[240:243], v[22:25]
	v_mfma_f32_16x16x32_bf16 v[14:17], v[154:157], v[248:251], v[14:17]
	v_mfma_f32_16x16x32_bf16 v[6:9], v[172:175], v[248:251], v[6:9]
	v_mfma_f32_16x16x32_bf16 v[66:69], v[176:179], v[204:207], v[66:69]
	v_mfma_f32_16x16x32_bf16 v[50:53], v[196:199], v[204:207], v[50:53]
	v_mfma_f32_16x16x32_bf16 v[42:45], v[176:179], v[212:215], v[42:45]
	v_mfma_f32_16x16x32_bf16 v[34:37], v[196:199], v[212:215], v[34:37]
	v_mfma_f32_16x16x32_bf16 v[26:29], v[176:179], v[220:223], v[26:29]
	v_mfma_f32_16x16x32_bf16 v[18:21], v[196:199], v[220:223], v[18:21]
	v_mfma_f32_16x16x32_bf16 v[10:13], v[176:179], v[244:247], v[10:13]
	v_mfma_f32_16x16x32_bf16 v[2:5], v[196:199], v[244:247], v[2:5]
	v_mfma_f32_16x16x32_bf16 v[66:69], v[180:183], v[208:211], v[66:69]
	v_mfma_f32_16x16x32_bf16 v[50:53], v[200:203], v[208:211], v[50:53]
	v_mfma_f32_16x16x32_bf16 v[42:45], v[180:183], v[216:219], v[42:45]
	v_mfma_f32_16x16x32_bf16 v[34:37], v[200:203], v[216:219], v[34:37]
	v_mfma_f32_16x16x32_bf16 v[26:29], v[180:183], v[240:243], v[26:29]
	v_mfma_f32_16x16x32_bf16 v[18:21], v[200:203], v[240:243], v[18:21]
	v_mfma_f32_16x16x32_bf16 v[10:13], v[180:183], v[248:251], v[10:13]
	v_mfma_f32_16x16x32_bf16 v[2:5], v[200:203], v[248:251], v[2:5]
	s_barrier
	s_add_i32 s35, 0, 0x19000
	v_add_u32_e32 v63, s35, v165
	s_add_i32 s55, 0, 0x1d000
	ds_read_b128 v[78:81], v63
	ds_read_b128 v[154:157], v63 offset:1024
	ds_read_b128 v[158:161], v63 offset:2048
	ds_read_b128 v[172:175], v63 offset:3072
	v_add_u32_e32 v63, s55, v165
	ds_read_b128 v[176:179], v63
	ds_read_b128 v[180:183], v63 offset:1024
	ds_read_b128 v[196:199], v63 offset:2048
	ds_read_b128 v[200:203], v63 offset:3072
	s_mov_b32 m0, s29
	ds_read_b128 v[204:207], v166 offset:36864
	ds_read_b128 v[208:211], v166 offset:37888
	ds_read_b128 v[212:215], v166 offset:38912
	ds_read_b128 v[216:219], v166 offset:39936
	ds_read_b128 v[220:223], v166 offset:40960
	ds_read_b128 v[240:243], v166 offset:41984
	ds_read_b128 v[244:247], v166 offset:43008
	ds_read_b128 v[248:251], v166 offset:44032
	global_load_lds_dwordx4 v59, s[14:15]
	s_mov_b32 m0, s33
	s_nop 0
	global_load_lds_dwordx4 v61, s[14:15]
	s_waitcnt vmcnt(8)
	s_waitcnt lgkmcnt(0)
	s_barrier
	s_waitcnt lgkmcnt(0)
	v_mfma_f32_16x16x32_bf16 v[142:145], v[78:81], v[204:207], v[142:145]
	v_mfma_f32_16x16x32_bf16 v[134:137], v[158:161], v[204:207], v[134:137]
	v_mfma_f32_16x16x32_bf16 v[126:129], v[78:81], v[212:215], v[126:129]
	v_mfma_f32_16x16x32_bf16 v[118:121], v[158:161], v[212:215], v[118:121]
	v_mfma_f32_16x16x32_bf16 v[110:113], v[78:81], v[220:223], v[110:113]
	v_mfma_f32_16x16x32_bf16 v[102:105], v[158:161], v[220:223], v[102:105]
	v_mfma_f32_16x16x32_bf16 v[94:97], v[78:81], v[244:247], v[94:97]
	v_mfma_f32_16x16x32_bf16 v[86:89], v[158:161], v[244:247], v[86:89]
	v_mfma_f32_16x16x32_bf16 v[142:145], v[154:157], v[208:211], v[142:145]
	v_mfma_f32_16x16x32_bf16 v[134:137], v[172:175], v[208:211], v[134:137]
	v_mfma_f32_16x16x32_bf16 v[126:129], v[154:157], v[216:219], v[126:129]
	v_mfma_f32_16x16x32_bf16 v[118:121], v[172:175], v[216:219], v[118:121]
	v_mfma_f32_16x16x32_bf16 v[110:113], v[154:157], v[240:243], v[110:113]
	v_mfma_f32_16x16x32_bf16 v[102:105], v[172:175], v[240:243], v[102:105]
	v_mfma_f32_16x16x32_bf16 v[94:97], v[154:157], v[248:251], v[94:97]
	v_mfma_f32_16x16x32_bf16 v[86:89], v[172:175], v[248:251], v[86:89]
	v_mfma_f32_16x16x32_bf16 v[138:141], v[176:179], v[204:207], v[138:141]
	v_mfma_f32_16x16x32_bf16 v[130:133], v[196:199], v[204:207], v[130:133]
	v_mfma_f32_16x16x32_bf16 v[122:125], v[176:179], v[212:215], v[122:125]
	v_mfma_f32_16x16x32_bf16 v[114:117], v[196:199], v[212:215], v[114:117]
	v_mfma_f32_16x16x32_bf16 v[106:109], v[176:179], v[220:223], v[106:109]
	v_mfma_f32_16x16x32_bf16 v[98:101], v[196:199], v[220:223], v[98:101]
	v_mfma_f32_16x16x32_bf16 v[90:93], v[176:179], v[244:247], v[90:93]
	v_mfma_f32_16x16x32_bf16 v[82:85], v[196:199], v[244:247], v[82:85]
	v_mfma_f32_16x16x32_bf16 v[138:141], v[180:183], v[208:211], v[138:141]
	v_mfma_f32_16x16x32_bf16 v[130:133], v[200:203], v[208:211], v[130:133]
	v_mfma_f32_16x16x32_bf16 v[122:125], v[180:183], v[216:219], v[122:125]
	v_mfma_f32_16x16x32_bf16 v[114:117], v[200:203], v[216:219], v[114:117]
	v_mfma_f32_16x16x32_bf16 v[106:109], v[180:183], v[240:243], v[106:109]
	v_mfma_f32_16x16x32_bf16 v[98:101], v[200:203], v[240:243], v[98:101]
	v_mfma_f32_16x16x32_bf16 v[90:93], v[180:183], v[248:251], v[90:93]
	v_mfma_f32_16x16x32_bf16 v[82:85], v[200:203], v[248:251], v[82:85]
	s_barrier
	s_add_i32 s14, s35, s17
	v_lshl_add_u64 v[230:231], v[192:193], 0, s[92:93]
	s_mov_b32 m0, s14
	ds_read_b128 v[204:207], v166 offset:53248
	ds_read_b128 v[208:211], v166 offset:54272
	ds_read_b128 v[212:215], v166 offset:55296
	ds_read_b128 v[216:219], v166 offset:56320
	ds_read_b128 v[220:223], v166 offset:57344
	ds_read_b128 v[240:243], v166 offset:58368
	ds_read_b128 v[244:247], v166 offset:59392
	ds_read_b128 v[248:251], v166 offset:60416
	global_load_lds_dwordx4 v[230:231], off
	v_lshl_add_u64 v[230:231], v[192:193], 0, s[4:5]
	s_add_i32 m0, s14, 0x2000
	s_add_i32 s14, s55, s17
	global_load_lds_dwordx4 v[230:231], off
	v_lshl_add_u64 v[230:231], v[192:193], 0, s[6:7]
	s_mov_b32 m0, s14
	v_lshl_add_u64 v[192:193], v[192:193], 0, s[8:9]
	global_load_lds_dwordx4 v[230:231], off
	s_add_i32 m0, s14, 0x2000
	v_lshl_add_u64 v[184:185], v[184:185], 0, s[92:93]
	global_load_lds_dwordx4 v[192:193], off
	v_lshl_add_u64 v[192:193], v[224:225], 0, s[92:93]
	s_mov_b32 m0, s80
	s_nop 0
	global_load_lds_dwordx4 v[192:193], off
	s_mov_b32 m0, s81
	s_nop 0
	global_load_lds_dwordx4 v[184:185], off
	s_waitcnt vmcnt(8)
	s_waitcnt lgkmcnt(0)
	s_barrier
	s_waitcnt lgkmcnt(0)
	v_mfma_f32_16x16x32_bf16 v[70:73], v[78:81], v[204:207], v[70:73]
	v_mfma_f32_16x16x32_bf16 v[54:57], v[158:161], v[204:207], v[54:57]
	s_add_i32 s34, s34, 2
	v_mfma_f32_16x16x32_bf16 v[46:49], v[78:81], v[212:215], v[46:49]
	s_add_u32 s40, s40, 0x100
	v_mfma_f32_16x16x32_bf16 v[38:41], v[158:161], v[212:215], v[38:41]
	s_addc_u32 s41, s41, 0
	v_mfma_f32_16x16x32_bf16 v[30:33], v[78:81], v[220:223], v[30:33]
	s_add_u32 s14, s70, s40
	v_mfma_f32_16x16x32_bf16 v[22:25], v[158:161], v[220:223], v[22:25]
	s_addc_u32 s15, s71, s41
	v_mfma_f32_16x16x32_bf16 v[14:17], v[78:81], v[244:247], v[14:17]
	s_add_u32 s35, s14, 0x100
	v_mfma_f32_16x16x32_bf16 v[6:9], v[158:161], v[244:247], v[6:9]
	s_addc_u32 s55, s15, 0
	v_mfma_f32_16x16x32_bf16 v[70:73], v[154:157], v[208:211], v[70:73]
	s_add_u32 s61, s1, s40
	v_mfma_f32_16x16x32_bf16 v[54:57], v[172:175], v[208:211], v[54:57]
	s_addc_u32 s69, s2, s41
	v_mfma_f32_16x16x32_bf16 v[46:49], v[154:157], v[216:219], v[46:49]
	s_cmpk_eq_i32 s40, 0x700
	v_mfma_f32_16x16x32_bf16 v[38:41], v[172:175], v[216:219], v[38:41]
	s_cselect_b64 vcc, -1, 0
	v_mfma_f32_16x16x32_bf16 v[30:33], v[154:157], v[240:243], v[30:33]
	s_and_b64 s[14:15], vcc, exec
	v_mfma_f32_16x16x32_bf16 v[22:25], v[172:175], v[240:243], v[22:25]
	s_cselect_b32 s15, s59, s55
	v_mfma_f32_16x16x32_bf16 v[14:17], v[154:157], v[248:251], v[14:17]
	s_cselect_b32 s14, s58, s35
	v_mfma_f32_16x16x32_bf16 v[6:9], v[172:175], v[248:251], v[6:9]
	s_cselect_b32 s73, s57, s69
	v_mfma_f32_16x16x32_bf16 v[66:69], v[176:179], v[204:207], v[66:69]
	s_cselect_b32 s72, s56, s61
	v_mfma_f32_16x16x32_bf16 v[50:53], v[196:199], v[204:207], v[50:53]
	s_add_i32 s35, 0, 0x11000
	v_mfma_f32_16x16x32_bf16 v[42:45], v[176:179], v[212:215], v[42:45]
	s_add_i32 s55, 0, 0x15000
	v_mfma_f32_16x16x32_bf16 v[34:37], v[196:199], v[212:215], v[34:37]
	v_mfma_f32_16x16x32_bf16 v[26:29], v[176:179], v[220:223], v[26:29]
	v_mfma_f32_16x16x32_bf16 v[18:21], v[196:199], v[220:223], v[18:21]
	v_mfma_f32_16x16x32_bf16 v[10:13], v[176:179], v[244:247], v[10:13]
	v_mfma_f32_16x16x32_bf16 v[2:5], v[196:199], v[244:247], v[2:5]
	v_mfma_f32_16x16x32_bf16 v[66:69], v[180:183], v[208:211], v[66:69]
	v_mfma_f32_16x16x32_bf16 v[50:53], v[200:203], v[208:211], v[50:53]
	v_mfma_f32_16x16x32_bf16 v[42:45], v[180:183], v[216:219], v[42:45]
	v_mfma_f32_16x16x32_bf16 v[34:37], v[200:203], v[216:219], v[34:37]
	v_mfma_f32_16x16x32_bf16 v[26:29], v[180:183], v[240:243], v[26:29]
	v_mfma_f32_16x16x32_bf16 v[18:21], v[200:203], v[240:243], v[18:21]
	v_mfma_f32_16x16x32_bf16 v[10:13], v[180:183], v[248:251], v[10:13]
	v_mfma_f32_16x16x32_bf16 v[2:5], v[200:203], v[248:251], v[2:5]
	s_barrier
	s_cmp_gt_u32 s34, 13
	s_cbranch_scc0 .LBB0_1339
	s_and_b64 vcc, exec, s[48:49]
	s_cbranch_vccnz .Lepi1_up
	s_setprio 1
	s_branch .Lepid_up

.Lepid_up:
	s_lshl_b32 s1, s60, 8
	s_or_b32 s14, s1, s84
	s_ashr_i32 s15, s14, 31
	s_lshl_b64 s[14:15], s[14:15], 2
	s_add_u32 s1, s74, s14
	s_addc_u32 s2, s75, s15
	s_ashr_i32 s69, s68, 31
	s_lshl_b64 s[14:15], s[68:69], 13
	s_add_u32 s14, s1, s14
	s_addc_u32 s15, s2, s15
	v_lshl_add_u64 v[78:79], s[14:15], 0, v[150:151]
	global_load_dwordx4 v[58:61], v[78:79], off offset:48
	global_load_dwordx4 v[62:65], v[78:79], off offset:32
	global_load_dwordx4 v[74:77], v[78:79], off offset:16
	s_nop 0
	global_load_dwordx4 v[78:81], v[78:79], off
	s_and_b64 vcc, exec, s[50:51]
	s_cbranch_vccz .LBB0_1342
	s_barrier

.LBB0_1462:
	s_andn2_b64 vcc, exec, s[44:45]
	s_cbranch_vccnz .Lprio_dn
	s_setprio 1
	s_branch .Lpriod_dn
.Lprio_dn:
	s_setprio 0
.Lpriod_dn:
	s_add_u32 s2, s56, 0x100
	s_addc_u32 s24, s57, 0
	s_add_u32 s56, s58, 0x40080
	s_waitcnt lgkmcnt(0)
	s_addc_u32 s57, s59, 0
	s_mov_b32 s25, -2
	s_add_u32 s14, s56, 0xfffc0080
	s_addc_u32 s15, s57, -1
	s_add_i32 s49, 0, 0x11000
	s_cmp_eq_u32 s25, 12
	s_cselect_b32 s15, s53, s15
	s_cselect_b32 s14, s52, s14
	v_add_u32_e32 v155, s49, v1
	s_cselect_b32 s35, s51, s24
	s_cselect_b32 s34, s50, s2
	s_add_i32 s55, 0, 0x15000
	ds_read_b128 v[156:159], v155
	ds_read_b128 v[160:163], v155 offset:1024
	ds_read_b128 v[164:167], v155 offset:2048
	ds_read_b128 v[168:171], v155 offset:3072
	v_add_u32_e32 v155, s55, v1
	ds_read_b128 v[172:175], v155
	ds_read_b128 v[176:179], v155 offset:1024
	ds_read_b128 v[180:183], v155 offset:2048
	ds_read_b128 v[196:199], v155 offset:3072
	v_lshl_add_u64 v[184:185], s[56:57], 0, v[152:153]
	s_add_i32 m0, s61, 0xd000
	ds_read_b128 v[200:203], v154 offset:4096
	ds_read_b128 v[204:207], v154 offset:5120
	ds_read_b128 v[208:211], v154 offset:6144
	ds_read_b128 v[212:215], v154 offset:7168
	ds_read_b128 v[216:219], v154 offset:8192
	ds_read_b128 v[220:223], v154 offset:9216
	ds_read_b128 v[240:243], v154 offset:10240
	ds_read_b128 v[244:247], v154 offset:11264
	global_load_lds_dwordx4 v[184:185], off
	v_lshl_add_u64 v[184:185], v[184:185], 0, s[82:83]
	s_add_i32 m0, s61, 0xf000
	s_nop 0
	global_load_lds_dwordx4 v[184:185], off
	s_waitcnt vmcnt(8)
	s_waitcnt lgkmcnt(0)
	s_barrier
	s_waitcnt lgkmcnt(0)
	v_mfma_f32_16x16x32_bf16 v[142:145], v[156:159], v[200:203], 0
	v_mfma_f32_16x16x32_bf16 v[138:141], v[164:167], v[200:203], 0
	v_mfma_f32_16x16x32_bf16 v[126:129], v[156:159], v[208:211], 0
	v_mfma_f32_16x16x32_bf16 v[122:125], v[164:167], v[208:211], 0
	v_mfma_f32_16x16x32_bf16 v[110:113], v[156:159], v[216:219], 0
	v_mfma_f32_16x16x32_bf16 v[106:109], v[164:167], v[216:219], 0
	v_mfma_f32_16x16x32_bf16 v[94:97], v[156:159], v[240:243], 0
	v_mfma_f32_16x16x32_bf16 v[90:93], v[164:167], v[240:243], 0
	v_mfma_f32_16x16x32_bf16 v[142:145], v[160:163], v[204:207], v[142:145]
	v_mfma_f32_16x16x32_bf16 v[138:141], v[168:171], v[204:207], v[138:141]
	v_mfma_f32_16x16x32_bf16 v[126:129], v[160:163], v[212:215], v[126:129]
	v_mfma_f32_16x16x32_bf16 v[122:125], v[168:171], v[212:215], v[122:125]
	v_mfma_f32_16x16x32_bf16 v[110:113], v[160:163], v[220:223], v[110:113]
	v_mfma_f32_16x16x32_bf16 v[106:109], v[168:171], v[220:223], v[106:109]
	v_mfma_f32_16x16x32_bf16 v[94:97], v[160:163], v[244:247], v[94:97]
	v_mfma_f32_16x16x32_bf16 v[90:93], v[168:171], v[244:247], v[90:93]
	v_mfma_f32_16x16x32_bf16 v[134:137], v[172:175], v[200:203], 0
	v_mfma_f32_16x16x32_bf16 v[130:133], v[180:183], v[200:203], 0
	v_mfma_f32_16x16x32_bf16 v[118:121], v[172:175], v[208:211], 0
	v_mfma_f32_16x16x32_bf16 v[114:117], v[180:183], v[208:211], 0
	v_mfma_f32_16x16x32_bf16 v[102:105], v[172:175], v[216:219], 0
	v_mfma_f32_16x16x32_bf16 v[98:101], v[180:183], v[216:219], 0
	v_mfma_f32_16x16x32_bf16 v[86:89], v[172:175], v[240:243], 0
	v_mfma_f32_16x16x32_bf16 v[82:85], v[180:183], v[240:243], 0
	v_mfma_f32_16x16x32_bf16 v[134:137], v[176:179], v[204:207], v[134:137]
	v_mfma_f32_16x16x32_bf16 v[130:133], v[196:199], v[204:207], v[130:133]
	v_mfma_f32_16x16x32_bf16 v[118:121], v[176:179], v[212:215], v[118:121]
	v_mfma_f32_16x16x32_bf16 v[114:117], v[196:199], v[212:215], v[114:117]
	v_mfma_f32_16x16x32_bf16 v[102:105], v[176:179], v[220:223], v[102:105]
	v_mfma_f32_16x16x32_bf16 v[98:101], v[196:199], v[220:223], v[98:101]
	v_mfma_f32_16x16x32_bf16 v[86:89], v[176:179], v[244:247], v[86:89]
	v_mfma_f32_16x16x32_bf16 v[82:85], v[196:199], v[244:247], v[82:85]
	s_barrier
	v_lshl_add_u64 v[184:185], s[34:35], 0, v[186:187]
	s_add_i32 s34, s49, s28
	s_mov_b32 m0, s34
	ds_read_b128 v[200:203], v154 offset:20480
	ds_read_b128 v[204:207], v154 offset:21504
	ds_read_b128 v[208:211], v154 offset:22528
	ds_read_b128 v[212:215], v154 offset:23552
	ds_read_b128 v[216:219], v154 offset:24576
	ds_read_b128 v[220:223], v154 offset:25600
	ds_read_b128 v[240:243], v154 offset:26624
	ds_read_b128 v[244:247], v154 offset:27648
	global_load_lds_dwordx4 v[184:185], off
	v_lshl_add_u64 v[192:193], v[184:185], 0, s[82:83]
	s_add_i32 m0, s34, 0x2000
	s_add_i32 s34, s55, s28
	global_load_lds_dwordx4 v[192:193], off
	v_lshl_add_u64 v[192:193], v[184:185], 0, s[64:65]
	s_mov_b32 m0, s34
	s_nop 0
	global_load_lds_dwordx4 v[192:193], off
	v_lshl_add_u64 v[192:193], v[184:185], 0, s[86:87]
	s_add_i32 m0, s34, 0x2000
	s_nop 0
	global_load_lds_dwordx4 v[192:193], off
	v_lshl_add_u64 v[192:193], s[14:15], 0, v[146:147]
	s_mov_b32 m0, s68
	v_lshl_add_u64 v[224:225], v[192:193], 0, s[82:83]
	global_load_lds_dwordx4 v[192:193], off
	s_mov_b32 m0, s69
	s_nop 0
	global_load_lds_dwordx4 v[224:225], off
	s_waitcnt vmcnt(8)
	s_waitcnt lgkmcnt(0)
	s_barrier
	s_waitcnt lgkmcnt(0)
	v_mfma_f32_16x16x32_bf16 v[78:81], v[156:159], v[200:203], 0
	v_mfma_f32_16x16x32_bf16 v[74:77], v[164:167], v[200:203], 0
	v_mfma_f32_16x16x32_bf16 v[62:65], v[156:159], v[208:211], 0
	v_mfma_f32_16x16x32_bf16 v[58:61], v[164:167], v[208:211], 0
	v_mfma_f32_16x16x32_bf16 v[46:49], v[156:159], v[216:219], 0
	v_mfma_f32_16x16x32_bf16 v[42:45], v[164:167], v[216:219], 0
	v_mfma_f32_16x16x32_bf16 v[30:33], v[156:159], v[240:243], 0
	v_mfma_f32_16x16x32_bf16 v[26:29], v[164:167], v[240:243], 0
	v_mfma_f32_16x16x32_bf16 v[78:81], v[160:163], v[204:207], v[78:81]
	v_mfma_f32_16x16x32_bf16 v[74:77], v[168:171], v[204:207], v[74:77]
	v_mfma_f32_16x16x32_bf16 v[62:65], v[160:163], v[212:215], v[62:65]
	v_mfma_f32_16x16x32_bf16 v[58:61], v[168:171], v[212:215], v[58:61]
	v_mfma_f32_16x16x32_bf16 v[46:49], v[160:163], v[220:223], v[46:49]
	v_mfma_f32_16x16x32_bf16 v[42:45], v[168:171], v[220:223], v[42:45]
	v_mfma_f32_16x16x32_bf16 v[30:33], v[160:163], v[244:247], v[30:33]
	v_mfma_f32_16x16x32_bf16 v[26:29], v[168:171], v[244:247], v[26:29]
	v_mfma_f32_16x16x32_bf16 v[70:73], v[172:175], v[200:203], 0
	v_mfma_f32_16x16x32_bf16 v[66:69], v[180:183], v[200:203], 0
	v_mfma_f32_16x16x32_bf16 v[54:57], v[172:175], v[208:211], 0
	v_mfma_f32_16x16x32_bf16 v[50:53], v[180:183], v[208:211], 0
	v_mfma_f32_16x16x32_bf16 v[38:41], v[172:175], v[216:219], 0
	v_mfma_f32_16x16x32_bf16 v[34:37], v[180:183], v[216:219], 0
	v_mfma_f32_16x16x32_bf16 v[22:25], v[172:175], v[240:243], 0
	v_mfma_f32_16x16x32_bf16 v[18:21], v[180:183], v[240:243], 0
	v_mfma_f32_16x16x32_bf16 v[70:73], v[176:179], v[204:207], v[70:73]
	v_mfma_f32_16x16x32_bf16 v[66:69], v[196:199], v[204:207], v[66:69]
	v_mfma_f32_16x16x32_bf16 v[54:57], v[176:179], v[212:215], v[54:57]
	v_mfma_f32_16x16x32_bf16 v[50:53], v[196:199], v[212:215], v[50:53]
	v_mfma_f32_16x16x32_bf16 v[38:41], v[176:179], v[220:223], v[38:41]
	v_mfma_f32_16x16x32_bf16 v[34:37], v[196:199], v[220:223], v[34:37]
	v_mfma_f32_16x16x32_bf16 v[22:25], v[176:179], v[244:247], v[22:25]
	v_mfma_f32_16x16x32_bf16 v[18:21], v[196:199], v[244:247], v[18:21]
	s_barrier
	s_add_i32 s14, 0, 0x19000
	v_add_u32_e32 v155, s14, v1
	s_add_i32 s15, 0, 0x1d000
	ds_read_b128 v[156:159], v155
	ds_read_b128 v[160:163], v155 offset:1024
	ds_read_b128 v[164:167], v155 offset:2048
	ds_read_b128 v[168:171], v155 offset:3072
	v_add_u32_e32 v155, s15, v1
	ds_read_b128 v[172:175], v155
	ds_read_b128 v[176:179], v155 offset:1024
	ds_read_b128 v[180:183], v155 offset:2048
	ds_read_b128 v[196:199], v155 offset:3072
	s_mov_b32 m0, s70
	v_lshl_add_u64 v[224:225], v[192:193], 0, s[64:65]
	ds_read_b128 v[200:203], v154 offset:36864
	ds_read_b128 v[204:207], v154 offset:37888
	ds_read_b128 v[208:211], v154 offset:38912
	ds_read_b128 v[212:215], v154 offset:39936
	ds_read_b128 v[216:219], v154 offset:40960
	ds_read_b128 v[220:223], v154 offset:41984
	ds_read_b128 v[240:243], v154 offset:43008
	ds_read_b128 v[244:247], v154 offset:44032
	global_load_lds_dwordx4 v[224:225], off
	v_lshl_add_u64 v[224:225], v[192:193], 0, s[86:87]
	s_mov_b32 m0, s71
	s_nop 0
	global_load_lds_dwordx4 v[224:225], off
	s_waitcnt vmcnt(8)
	s_waitcnt lgkmcnt(0)
	s_barrier
	s_waitcnt lgkmcnt(0)
	v_mfma_f32_16x16x32_bf16 v[142:145], v[156:159], v[200:203], v[142:145]
	v_mfma_f32_16x16x32_bf16 v[138:141], v[164:167], v[200:203], v[138:141]
	v_mfma_f32_16x16x32_bf16 v[126:129], v[156:159], v[208:211], v[126:129]
	v_mfma_f32_16x16x32_bf16 v[122:125], v[164:167], v[208:211], v[122:125]
	v_mfma_f32_16x16x32_bf16 v[110:113], v[156:159], v[216:219], v[110:113]
	v_mfma_f32_16x16x32_bf16 v[106:109], v[164:167], v[216:219], v[106:109]
	v_mfma_f32_16x16x32_bf16 v[94:97], v[156:159], v[240:243], v[94:97]
	v_mfma_f32_16x16x32_bf16 v[90:93], v[164:167], v[240:243], v[90:93]
	v_mfma_f32_16x16x32_bf16 v[142:145], v[160:163], v[204:207], v[142:145]
	v_mfma_f32_16x16x32_bf16 v[138:141], v[168:171], v[204:207], v[138:141]
	v_mfma_f32_16x16x32_bf16 v[126:129], v[160:163], v[212:215], v[126:129]
	v_mfma_f32_16x16x32_bf16 v[122:125], v[168:171], v[212:215], v[122:125]
	v_mfma_f32_16x16x32_bf16 v[110:113], v[160:163], v[220:223], v[110:113]
	v_mfma_f32_16x16x32_bf16 v[106:109], v[168:171], v[220:223], v[106:109]
	v_mfma_f32_16x16x32_bf16 v[94:97], v[160:163], v[244:247], v[94:97]
	v_mfma_f32_16x16x32_bf16 v[90:93], v[168:171], v[244:247], v[90:93]
	v_mfma_f32_16x16x32_bf16 v[134:137], v[172:175], v[200:203], v[134:137]
	v_mfma_f32_16x16x32_bf16 v[130:133], v[180:183], v[200:203], v[130:133]
	v_mfma_f32_16x16x32_bf16 v[118:121], v[172:175], v[208:211], v[118:121]
	v_mfma_f32_16x16x32_bf16 v[114:117], v[180:183], v[208:211], v[114:117]
	v_mfma_f32_16x16x32_bf16 v[102:105], v[172:175], v[216:219], v[102:105]
	v_mfma_f32_16x16x32_bf16 v[98:101], v[180:183], v[216:219], v[98:101]
	v_mfma_f32_16x16x32_bf16 v[86:89], v[172:175], v[240:243], v[86:89]
	v_mfma_f32_16x16x32_bf16 v[82:85], v[180:183], v[240:243], v[82:85]
	v_mfma_f32_16x16x32_bf16 v[134:137], v[176:179], v[204:207], v[134:137]
	v_mfma_f32_16x16x32_bf16 v[130:133], v[196:199], v[204:207], v[130:133]
	v_mfma_f32_16x16x32_bf16 v[118:121], v[176:179], v[212:215], v[118:121]
	v_mfma_f32_16x16x32_bf16 v[114:117], v[196:199], v[212:215], v[114:117]
	v_mfma_f32_16x16x32_bf16 v[102:105], v[176:179], v[220:223], v[102:105]
	v_mfma_f32_16x16x32_bf16 v[98:101], v[196:199], v[220:223], v[98:101]
	v_mfma_f32_16x16x32_bf16 v[86:89], v[176:179], v[244:247], v[86:89]
	v_mfma_f32_16x16x32_bf16 v[82:85], v[196:199], v[244:247], v[82:85]
	s_barrier
	s_add_i32 s14, s14, s28
	v_lshl_add_u64 v[224:225], v[184:185], 0, s[92:93]
	s_mov_b32 m0, s14
	ds_read_b128 v[200:203], v154 offset:53248
	ds_read_b128 v[204:207], v154 offset:54272
	ds_read_b128 v[208:211], v154 offset:55296
	ds_read_b128 v[212:215], v154 offset:56320
	ds_read_b128 v[216:219], v154 offset:57344
	ds_read_b128 v[220:223], v154 offset:58368
	ds_read_b128 v[240:243], v154 offset:59392
	ds_read_b128 v[244:247], v154 offset:60416
	global_load_lds_dwordx4 v[224:225], off
	v_lshl_add_u64 v[224:225], v[184:185], 0, s[4:5]
	s_add_i32 m0, s14, 0x2000
	s_add_i32 s14, s15, s28
	global_load_lds_dwordx4 v[224:225], off
	v_lshl_add_u64 v[224:225], v[184:185], 0, s[6:7]
	s_mov_b32 m0, s14
	v_lshl_add_u64 v[184:185], v[184:185], 0, s[8:9]
	global_load_lds_dwordx4 v[224:225], off
	s_add_i32 m0, s14, 0x2000
	s_nop 0
	global_load_lds_dwordx4 v[184:185], off
	v_lshl_add_u64 v[184:185], v[192:193], 0, s[92:93]
	s_mov_b32 m0, s75
	s_nop 0
	global_load_lds_dwordx4 v[184:185], off
	v_lshl_add_u64 v[184:185], v[192:193], 0, s[4:5]
	s_mov_b32 m0, s76
	s_nop 0
	global_load_lds_dwordx4 v[184:185], off
	s_waitcnt vmcnt(8)
	s_waitcnt lgkmcnt(0)
	s_barrier
	s_waitcnt lgkmcnt(0)
	v_mfma_f32_16x16x32_bf16 v[78:81], v[156:159], v[200:203], v[78:81]
	v_mfma_f32_16x16x32_bf16 v[74:77], v[164:167], v[200:203], v[74:77]
	s_add_i32 s25, s25, 2
	v_mfma_f32_16x16x32_bf16 v[62:65], v[156:159], v[208:211], v[62:65]
	s_add_u32 s2, s2, 0x100
	v_mfma_f32_16x16x32_bf16 v[58:61], v[164:167], v[208:211], v[58:61]
	s_addc_u32 s24, s24, 0
	v_mfma_f32_16x16x32_bf16 v[46:49], v[156:159], v[216:219], v[46:49]
	s_add_u32 s56, s56, 0x100
	v_mfma_f32_16x16x32_bf16 v[42:45], v[164:167], v[216:219], v[42:45]
	s_addc_u32 s57, s57, 0
	v_mfma_f32_16x16x32_bf16 v[30:33], v[156:159], v[240:243], v[30:33]
	s_add_u32 s14, s56, 0xfffc0080
	v_mfma_f32_16x16x32_bf16 v[26:29], v[164:167], v[240:243], v[26:29]
	s_addc_u32 s15, s57, -1
	v_mfma_f32_16x16x32_bf16 v[78:81], v[160:163], v[204:207], v[78:81]
	s_add_i32 s49, 0, 0x11000
	v_mfma_f32_16x16x32_bf16 v[74:77], v[168:171], v[204:207], v[74:77]
	s_cmp_eq_u32 s25, 12
	v_mfma_f32_16x16x32_bf16 v[62:65], v[160:163], v[212:215], v[62:65]
	s_cselect_b32 s15, s53, s15
	v_mfma_f32_16x16x32_bf16 v[58:61], v[168:171], v[212:215], v[58:61]
	s_cselect_b32 s14, s52, s14
	v_mfma_f32_16x16x32_bf16 v[46:49], v[160:163], v[220:223], v[46:49]
	s_cselect_b32 s35, s51, s24
	v_mfma_f32_16x16x32_bf16 v[42:45], v[168:171], v[220:223], v[42:45]
	s_cselect_b32 s34, s50, s2
	v_mfma_f32_16x16x32_bf16 v[30:33], v[160:163], v[244:247], v[30:33]
	s_add_i32 s55, 0, 0x15000
	v_mfma_f32_16x16x32_bf16 v[26:29], v[168:171], v[244:247], v[26:29]
	v_mfma_f32_16x16x32_bf16 v[70:73], v[172:175], v[200:203], v[70:73]
	v_mfma_f32_16x16x32_bf16 v[66:69], v[180:183], v[200:203], v[66:69]
	v_mfma_f32_16x16x32_bf16 v[54:57], v[172:175], v[208:211], v[54:57]
	v_mfma_f32_16x16x32_bf16 v[50:53], v[180:183], v[208:211], v[50:53]
	v_mfma_f32_16x16x32_bf16 v[38:41], v[172:175], v[216:219], v[38:41]
	v_mfma_f32_16x16x32_bf16 v[34:37], v[180:183], v[216:219], v[34:37]
	v_mfma_f32_16x16x32_bf16 v[22:25], v[172:175], v[240:243], v[22:25]
	v_mfma_f32_16x16x32_bf16 v[18:21], v[180:183], v[240:243], v[18:21]
	v_mfma_f32_16x16x32_bf16 v[70:73], v[176:179], v[204:207], v[70:73]
	v_mfma_f32_16x16x32_bf16 v[66:69], v[196:199], v[204:207], v[66:69]
	v_mfma_f32_16x16x32_bf16 v[54:57], v[176:179], v[212:215], v[54:57]
	v_mfma_f32_16x16x32_bf16 v[50:53], v[196:199], v[212:215], v[50:53]
	v_mfma_f32_16x16x32_bf16 v[38:41], v[176:179], v[220:223], v[38:41]
	v_mfma_f32_16x16x32_bf16 v[34:37], v[196:199], v[220:223], v[34:37]
	v_mfma_f32_16x16x32_bf16 v[22:25], v[176:179], v[244:247], v[22:25]
	v_mfma_f32_16x16x32_bf16 v[18:21], v[196:199], v[244:247], v[18:21]
	s_barrier
.LBB0_1463:
	v_add_u32_e32 v155, s49, v1
	ds_read_b128 v[156:159], v155
	ds_read_b128 v[160:163], v155 offset:1024
	ds_read_b128 v[164:167], v155 offset:2048
	ds_read_b128 v[168:171], v155 offset:3072
	v_add_u32_e32 v155, s55, v1
	ds_read_b128 v[172:175], v155
	ds_read_b128 v[176:179], v155 offset:1024
	ds_read_b128 v[180:183], v155 offset:2048
	ds_read_b128 v[196:199], v155 offset:3072
	v_lshl_add_u64 v[184:185], s[56:57], 0, v[152:153]
	s_add_i32 m0, s61, 0xd000
	ds_read_b128 v[200:203], v154 offset:4096
	ds_read_b128 v[204:207], v154 offset:5120
	ds_read_b128 v[208:211], v154 offset:6144
	ds_read_b128 v[212:215], v154 offset:7168
	ds_read_b128 v[216:219], v154 offset:8192
	ds_read_b128 v[220:223], v154 offset:9216
	ds_read_b128 v[240:243], v154 offset:10240
	ds_read_b128 v[244:247], v154 offset:11264
	global_load_lds_dwordx4 v[184:185], off
	v_lshl_add_u64 v[184:185], v[184:185], 0, s[82:83]
	s_add_i32 m0, s61, 0xf000
	s_nop 0
	global_load_lds_dwordx4 v[184:185], off
	s_waitcnt vmcnt(8)
	s_waitcnt lgkmcnt(0)
	s_barrier
	s_waitcnt lgkmcnt(0)
	v_mfma_f32_16x16x32_bf16 v[142:145], v[156:159], v[200:203], v[142:145]
	v_mfma_f32_16x16x32_bf16 v[138:141], v[164:167], v[200:203], v[138:141]
	v_mfma_f32_16x16x32_bf16 v[126:129], v[156:159], v[208:211], v[126:129]
	v_mfma_f32_16x16x32_bf16 v[122:125], v[164:167], v[208:211], v[122:125]
	v_mfma_f32_16x16x32_bf16 v[110:113], v[156:159], v[216:219], v[110:113]
	v_mfma_f32_16x16x32_bf16 v[106:109], v[164:167], v[216:219], v[106:109]
	v_mfma_f32_16x16x32_bf16 v[94:97], v[156:159], v[240:243], v[94:97]
	v_mfma_f32_16x16x32_bf16 v[90:93], v[164:167], v[240:243], v[90:93]
	v_mfma_f32_16x16x32_bf16 v[142:145], v[160:163], v[204:207], v[142:145]
	v_mfma_f32_16x16x32_bf16 v[138:141], v[168:171], v[204:207], v[138:141]
	v_mfma_f32_16x16x32_bf16 v[126:129], v[160:163], v[212:215], v[126:129]
	v_mfma_f32_16x16x32_bf16 v[122:125], v[168:171], v[212:215], v[122:125]
	v_mfma_f32_16x16x32_bf16 v[110:113], v[160:163], v[220:223], v[110:113]
	v_mfma_f32_16x16x32_bf16 v[106:109], v[168:171], v[220:223], v[106:109]
	v_mfma_f32_16x16x32_bf16 v[94:97], v[160:163], v[244:247], v[94:97]
	v_mfma_f32_16x16x32_bf16 v[90:93], v[168:171], v[244:247], v[90:93]
	v_mfma_f32_16x16x32_bf16 v[134:137], v[172:175], v[200:203], v[134:137]
	v_mfma_f32_16x16x32_bf16 v[130:133], v[180:183], v[200:203], v[130:133]
	v_mfma_f32_16x16x32_bf16 v[118:121], v[172:175], v[208:211], v[118:121]
	v_mfma_f32_16x16x32_bf16 v[114:117], v[180:183], v[208:211], v[114:117]
	v_mfma_f32_16x16x32_bf16 v[102:105], v[172:175], v[216:219], v[102:105]
	v_mfma_f32_16x16x32_bf16 v[98:101], v[180:183], v[216:219], v[98:101]
	v_mfma_f32_16x16x32_bf16 v[86:89], v[172:175], v[240:243], v[86:89]
	v_mfma_f32_16x16x32_bf16 v[82:85], v[180:183], v[240:243], v[82:85]
	v_mfma_f32_16x16x32_bf16 v[134:137], v[176:179], v[204:207], v[134:137]
	v_mfma_f32_16x16x32_bf16 v[130:133], v[196:199], v[204:207], v[130:133]
	v_mfma_f32_16x16x32_bf16 v[118:121], v[176:179], v[212:215], v[118:121]
	v_mfma_f32_16x16x32_bf16 v[114:117], v[196:199], v[212:215], v[114:117]
	v_mfma_f32_16x16x32_bf16 v[102:105], v[176:179], v[220:223], v[102:105]
	v_mfma_f32_16x16x32_bf16 v[98:101], v[196:199], v[220:223], v[98:101]
	v_mfma_f32_16x16x32_bf16 v[86:89], v[176:179], v[244:247], v[86:89]
	v_mfma_f32_16x16x32_bf16 v[82:85], v[196:199], v[244:247], v[82:85]
	s_barrier
	v_lshl_add_u64 v[184:185], s[34:35], 0, v[186:187]
	s_add_i32 s34, s49, s28
	s_mov_b32 m0, s34
	ds_read_b128 v[200:203], v154 offset:20480
	ds_read_b128 v[204:207], v154 offset:21504
	ds_read_b128 v[208:211], v154 offset:22528
	ds_read_b128 v[212:215], v154 offset:23552
	ds_read_b128 v[216:219], v154 offset:24576
	ds_read_b128 v[220:223], v154 offset:25600
	ds_read_b128 v[240:243], v154 offset:26624
	ds_read_b128 v[244:247], v154 offset:27648
	global_load_lds_dwordx4 v[184:185], off
	v_lshl_add_u64 v[192:193], v[184:185], 0, s[82:83]
	s_add_i32 m0, s34, 0x2000
	s_add_i32 s34, s55, s28
	global_load_lds_dwordx4 v[192:193], off
	v_lshl_add_u64 v[192:193], v[184:185], 0, s[64:65]
	s_mov_b32 m0, s34
	s_nop 0
	global_load_lds_dwordx4 v[192:193], off
	v_lshl_add_u64 v[192:193], v[184:185], 0, s[86:87]
	s_add_i32 m0, s34, 0x2000
	s_nop 0
	global_load_lds_dwordx4 v[192:193], off
	v_lshl_add_u64 v[192:193], s[14:15], 0, v[146:147]
	s_mov_b32 m0, s68
	v_lshl_add_u64 v[224:225], v[192:193], 0, s[82:83]
	global_load_lds_dwordx4 v[192:193], off
	s_mov_b32 m0, s69
	s_nop 0
	global_load_lds_dwordx4 v[224:225], off
	s_waitcnt vmcnt(8)
	s_waitcnt lgkmcnt(0)
	s_barrier
	s_waitcnt lgkmcnt(0)
	v_mfma_f32_16x16x32_bf16 v[78:81], v[156:159], v[200:203], v[78:81]
	v_mfma_f32_16x16x32_bf16 v[74:77], v[164:167], v[200:203], v[74:77]
	v_mfma_f32_16x16x32_bf16 v[62:65], v[156:159], v[208:211], v[62:65]
	v_mfma_f32_16x16x32_bf16 v[58:61], v[164:167], v[208:211], v[58:61]
	v_mfma_f32_16x16x32_bf16 v[46:49], v[156:159], v[216:219], v[46:49]
	v_mfma_f32_16x16x32_bf16 v[42:45], v[164:167], v[216:219], v[42:45]
	v_mfma_f32_16x16x32_bf16 v[30:33], v[156:159], v[240:243], v[30:33]
	v_mfma_f32_16x16x32_bf16 v[26:29], v[164:167], v[240:243], v[26:29]
	v_mfma_f32_16x16x32_bf16 v[78:81], v[160:163], v[204:207], v[78:81]
	v_mfma_f32_16x16x32_bf16 v[74:77], v[168:171], v[204:207], v[74:77]
	v_mfma_f32_16x16x32_bf16 v[62:65], v[160:163], v[212:215], v[62:65]
	v_mfma_f32_16x16x32_bf16 v[58:61], v[168:171], v[212:215], v[58:61]
	v_mfma_f32_16x16x32_bf16 v[46:49], v[160:163], v[220:223], v[46:49]
	v_mfma_f32_16x16x32_bf16 v[42:45], v[168:171], v[220:223], v[42:45]
	v_mfma_f32_16x16x32_bf16 v[30:33], v[160:163], v[244:247], v[30:33]
	v_mfma_f32_16x16x32_bf16 v[26:29], v[168:171], v[244:247], v[26:29]
	v_mfma_f32_16x16x32_bf16 v[70:73], v[172:175], v[200:203], v[70:73]
	v_mfma_f32_16x16x32_bf16 v[66:69], v[180:183], v[200:203], v[66:69]
	v_mfma_f32_16x16x32_bf16 v[54:57], v[172:175], v[208:211], v[54:57]
	v_mfma_f32_16x16x32_bf16 v[50:53], v[180:183], v[208:211], v[50:53]
	v_mfma_f32_16x16x32_bf16 v[38:41], v[172:175], v[216:219], v[38:41]
	v_mfma_f32_16x16x32_bf16 v[34:37], v[180:183], v[216:219], v[34:37]
	v_mfma_f32_16x16x32_bf16 v[22:25], v[172:175], v[240:243], v[22:25]
	v_mfma_f32_16x16x32_bf16 v[18:21], v[180:183], v[240:243], v[18:21]
	v_mfma_f32_16x16x32_bf16 v[70:73], v[176:179], v[204:207], v[70:73]
	v_mfma_f32_16x16x32_bf16 v[66:69], v[196:199], v[204:207], v[66:69]
	v_mfma_f32_16x16x32_bf16 v[54:57], v[176:179], v[212:215], v[54:57]
	v_mfma_f32_16x16x32_bf16 v[50:53], v[196:199], v[212:215], v[50:53]
	v_mfma_f32_16x16x32_bf16 v[38:41], v[176:179], v[220:223], v[38:41]
	v_mfma_f32_16x16x32_bf16 v[34:37], v[196:199], v[220:223], v[34:37]
	v_mfma_f32_16x16x32_bf16 v[22:25], v[176:179], v[244:247], v[22:25]
	v_mfma_f32_16x16x32_bf16 v[18:21], v[196:199], v[244:247], v[18:21]
	s_barrier
	s_add_i32 s14, 0, 0x19000
	v_add_u32_e32 v155, s14, v1
	s_add_i32 s15, 0, 0x1d000
	ds_read_b128 v[156:159], v155
	ds_read_b128 v[160:163], v155 offset:1024
	ds_read_b128 v[164:167], v155 offset:2048
	ds_read_b128 v[168:171], v155 offset:3072
	v_add_u32_e32 v155, s15, v1
	ds_read_b128 v[172:175], v155
	ds_read_b128 v[176:179], v155 offset:1024
	ds_read_b128 v[180:183], v155 offset:2048
	ds_read_b128 v[196:199], v155 offset:3072
	s_mov_b32 m0, s70
	v_lshl_add_u64 v[224:225], v[192:193], 0, s[64:65]
	ds_read_b128 v[200:203], v154 offset:36864
	ds_read_b128 v[204:207], v154 offset:37888
	ds_read_b128 v[208:211], v154 offset:38912
	ds_read_b128 v[212:215], v154 offset:39936
	ds_read_b128 v[216:219], v154 offset:40960
	ds_read_b128 v[220:223], v154 offset:41984
	ds_read_b128 v[240:243], v154 offset:43008
	ds_read_b128 v[244:247], v154 offset:44032
	global_load_lds_dwordx4 v[224:225], off
	v_lshl_add_u64 v[224:225], v[192:193], 0, s[86:87]
	s_mov_b32 m0, s71
	s_nop 0
	global_load_lds_dwordx4 v[224:225], off
	s_waitcnt vmcnt(8)
	s_waitcnt lgkmcnt(0)
	s_barrier
	s_waitcnt lgkmcnt(0)
	v_mfma_f32_16x16x32_bf16 v[142:145], v[156:159], v[200:203], v[142:145]
	v_mfma_f32_16x16x32_bf16 v[138:141], v[164:167], v[200:203], v[138:141]
	v_mfma_f32_16x16x32_bf16 v[126:129], v[156:159], v[208:211], v[126:129]
	v_mfma_f32_16x16x32_bf16 v[122:125], v[164:167], v[208:211], v[122:125]
	v_mfma_f32_16x16x32_bf16 v[110:113], v[156:159], v[216:219], v[110:113]
	v_mfma_f32_16x16x32_bf16 v[106:109], v[164:167], v[216:219], v[106:109]
	v_mfma_f32_16x16x32_bf16 v[94:97], v[156:159], v[240:243], v[94:97]
	v_mfma_f32_16x16x32_bf16 v[90:93], v[164:167], v[240:243], v[90:93]
	v_mfma_f32_16x16x32_bf16 v[142:145], v[160:163], v[204:207], v[142:145]
	v_mfma_f32_16x16x32_bf16 v[138:141], v[168:171], v[204:207], v[138:141]
	v_mfma_f32_16x16x32_bf16 v[126:129], v[160:163], v[212:215], v[126:129]
	v_mfma_f32_16x16x32_bf16 v[122:125], v[168:171], v[212:215], v[122:125]
	v_mfma_f32_16x16x32_bf16 v[110:113], v[160:163], v[220:223], v[110:113]
	v_mfma_f32_16x16x32_bf16 v[106:109], v[168:171], v[220:223], v[106:109]
	v_mfma_f32_16x16x32_bf16 v[94:97], v[160:163], v[244:247], v[94:97]
	v_mfma_f32_16x16x32_bf16 v[90:93], v[168:171], v[244:247], v[90:93]
	v_mfma_f32_16x16x32_bf16 v[134:137], v[172:175], v[200:203], v[134:137]
	v_mfma_f32_16x16x32_bf16 v[130:133], v[180:183], v[200:203], v[130:133]
	v_mfma_f32_16x16x32_bf16 v[118:121], v[172:175], v[208:211], v[118:121]
	v_mfma_f32_16x16x32_bf16 v[114:117], v[180:183], v[208:211], v[114:117]
	v_mfma_f32_16x16x32_bf16 v[102:105], v[172:175], v[216:219], v[102:105]
	v_mfma_f32_16x16x32_bf16 v[98:101], v[180:183], v[216:219], v[98:101]
	v_mfma_f32_16x16x32_bf16 v[86:89], v[172:175], v[240:243], v[86:89]
	v_mfma_f32_16x16x32_bf16 v[82:85], v[180:183], v[240:243], v[82:85]
	v_mfma_f32_16x16x32_bf16 v[134:137], v[176:179], v[204:207], v[134:137]
	v_mfma_f32_16x16x32_bf16 v[130:133], v[196:199], v[204:207], v[130:133]
	v_mfma_f32_16x16x32_bf16 v[118:121], v[176:179], v[212:215], v[118:121]
	v_mfma_f32_16x16x32_bf16 v[114:117], v[196:199], v[212:215], v[114:117]
	v_mfma_f32_16x16x32_bf16 v[102:105], v[176:179], v[220:223], v[102:105]
	v_mfma_f32_16x16x32_bf16 v[98:101], v[196:199], v[220:223], v[98:101]
	v_mfma_f32_16x16x32_bf16 v[86:89], v[176:179], v[244:247], v[86:89]
	v_mfma_f32_16x16x32_bf16 v[82:85], v[196:199], v[244:247], v[82:85]
	s_barrier
	s_add_i32 s14, s14, s28
	v_lshl_add_u64 v[224:225], v[184:185], 0, s[92:93]
	s_mov_b32 m0, s14
	ds_read_b128 v[200:203], v154 offset:53248
	ds_read_b128 v[204:207], v154 offset:54272
	ds_read_b128 v[208:211], v154 offset:55296
	ds_read_b128 v[212:215], v154 offset:56320
	ds_read_b128 v[216:219], v154 offset:57344
	ds_read_b128 v[220:223], v154 offset:58368
	ds_read_b128 v[240:243], v154 offset:59392
	ds_read_b128 v[244:247], v154 offset:60416
	global_load_lds_dwordx4 v[224:225], off
	v_lshl_add_u64 v[224:225], v[184:185], 0, s[4:5]
	s_add_i32 m0, s14, 0x2000
	s_add_i32 s14, s15, s28
	global_load_lds_dwordx4 v[224:225], off
	v_lshl_add_u64 v[224:225], v[184:185], 0, s[6:7]
	s_mov_b32 m0, s14
	v_lshl_add_u64 v[184:185], v[184:185], 0, s[8:9]
	global_load_lds_dwordx4 v[224:225], off
	s_add_i32 m0, s14, 0x2000
	s_nop 0
	global_load_lds_dwordx4 v[184:185], off
	v_lshl_add_u64 v[184:185], v[192:193], 0, s[92:93]
	s_mov_b32 m0, s75
	s_nop 0
	global_load_lds_dwordx4 v[184:185], off
	v_lshl_add_u64 v[184:185], v[192:193], 0, s[4:5]
	s_mov_b32 m0, s76
	s_nop 0
	global_load_lds_dwordx4 v[184:185], off
	s_waitcnt vmcnt(8)
	s_waitcnt lgkmcnt(0)
	s_barrier
	s_waitcnt lgkmcnt(0)
	v_mfma_f32_16x16x32_bf16 v[78:81], v[156:159], v[200:203], v[78:81]
	v_mfma_f32_16x16x32_bf16 v[74:77], v[164:167], v[200:203], v[74:77]
	s_add_i32 s25, s25, 2
	v_mfma_f32_16x16x32_bf16 v[62:65], v[156:159], v[208:211], v[62:65]
	s_add_u32 s2, s2, 0x100
	v_mfma_f32_16x16x32_bf16 v[58:61], v[164:167], v[208:211], v[58:61]
	s_addc_u32 s24, s24, 0
	v_mfma_f32_16x16x32_bf16 v[46:49], v[156:159], v[216:219], v[46:49]
	s_add_u32 s56, s56, 0x100
	v_mfma_f32_16x16x32_bf16 v[42:45], v[164:167], v[216:219], v[42:45]
	s_addc_u32 s57, s57, 0
	v_mfma_f32_16x16x32_bf16 v[30:33], v[156:159], v[240:243], v[30:33]
	s_add_u32 s14, s56, 0xfffc0080
	v_mfma_f32_16x16x32_bf16 v[26:29], v[164:167], v[240:243], v[26:29]
	s_addc_u32 s15, s57, -1
	v_mfma_f32_16x16x32_bf16 v[78:81], v[160:163], v[204:207], v[78:81]
	s_add_i32 s49, 0, 0x11000
	v_mfma_f32_16x16x32_bf16 v[74:77], v[168:171], v[204:207], v[74:77]
	s_cmp_eq_u32 s25, 12
	v_mfma_f32_16x16x32_bf16 v[62:65], v[160:163], v[212:215], v[62:65]
	s_cselect_b32 s15, s53, s15
	v_mfma_f32_16x16x32_bf16 v[58:61], v[168:171], v[212:215], v[58:61]
	s_cselect_b32 s14, s52, s14
	v_mfma_f32_16x16x32_bf16 v[46:49], v[160:163], v[220:223], v[46:49]
	s_cselect_b32 s35, s51, s24
	v_mfma_f32_16x16x32_bf16 v[42:45], v[168:171], v[220:223], v[42:45]
	s_cselect_b32 s34, s50, s2
	v_mfma_f32_16x16x32_bf16 v[30:33], v[160:163], v[244:247], v[30:33]
	s_add_i32 s55, 0, 0x15000
	v_mfma_f32_16x16x32_bf16 v[26:29], v[168:171], v[244:247], v[26:29]
	v_mfma_f32_16x16x32_bf16 v[70:73], v[172:175], v[200:203], v[70:73]
	v_mfma_f32_16x16x32_bf16 v[66:69], v[180:183], v[200:203], v[66:69]
	v_mfma_f32_16x16x32_bf16 v[54:57], v[172:175], v[208:211], v[54:57]
	v_mfma_f32_16x16x32_bf16 v[50:53], v[180:183], v[208:211], v[50:53]
	v_mfma_f32_16x16x32_bf16 v[38:41], v[172:175], v[216:219], v[38:41]
	v_mfma_f32_16x16x32_bf16 v[34:37], v[180:183], v[216:219], v[34:37]
	v_mfma_f32_16x16x32_bf16 v[22:25], v[172:175], v[240:243], v[22:25]
	v_mfma_f32_16x16x32_bf16 v[18:21], v[180:183], v[240:243], v[18:21]
	v_mfma_f32_16x16x32_bf16 v[70:73], v[176:179], v[204:207], v[70:73]
	v_mfma_f32_16x16x32_bf16 v[66:69], v[196:199], v[204:207], v[66:69]
	v_mfma_f32_16x16x32_bf16 v[54:57], v[176:179], v[212:215], v[54:57]
	v_mfma_f32_16x16x32_bf16 v[50:53], v[196:199], v[212:215], v[50:53]
	v_mfma_f32_16x16x32_bf16 v[38:41], v[176:179], v[220:223], v[38:41]
	v_mfma_f32_16x16x32_bf16 v[34:37], v[196:199], v[220:223], v[34:37]
	v_mfma_f32_16x16x32_bf16 v[22:25], v[176:179], v[244:247], v[22:25]
	v_mfma_f32_16x16x32_bf16 v[18:21], v[196:199], v[244:247], v[18:21]
	s_barrier
	s_cmp_gt_u32 s25, 13
	s_cbranch_scc0 .LBB0_1463
	s_and_b64 vcc, exec, s[44:45]
	s_cbranch_vccnz .Lepi1_dn
	s_setprio 1
	s_branch .Lepid_dn

.Lepid_dn:
	s_and_b64 vcc, exec, s[46:47]
	s_cbranch_vccz .LBB0_1466
	s_barrier
